# baseline (speedup 1.0000x reference)
_Z8gat_mainPKiPKDF16_PKfS4_Pf:
	s_load_dwordx8 s[24:31], s[0:1], 0x0
	s_load_dwordx2 s[12:13], s[0:1], 0x20
	v_and_b32_e32 v2, 63, v0
	v_readfirstlane_b32 s16, v0
	v_lshlrev_b32_e32 v1, 4, v2
	s_lshr_b32 s16, s16, 6
	s_and_b32 s17, s2, 7
	s_lshr_b32 s18, s2, 3
	s_lshr_b32 s19, s18, 3
	s_add_u32 s19, s19, s18
	s_and_b32 s19, s19, 7
	s_lshr_b32 s20, s16, 2
	s_and_b32 s21, s16, 3
	s_lshl_b32 s22, s16, 16
	s_lshl_b32 s23, s16, 12
	s_waitcnt lgkmcnt(0)
	s_lshl_b32 s3, s17, 24
	s_lshl_b32 s57, s18, 19
	s_add_u32 s3, s3, s57
	s_add_u32 s4, s24, s3
	s_addc_u32 s5, s25, 0
	s_and_b32 s5, s5, 0xffff
	s_mov_b32 s6, 0x80000
	s_mov_b32 s7, 0x20000
	s_lshl_b32 s3, s17, 18
	s_add_u32 s8, s26, s3
	s_addc_u32 s9, s27, 0
	s_and_b32 s9, s9, 0xffff
	s_mov_b32 s10, 0x40000
	s_mov_b32 s11, 0x20000
	s_lshl_b32 s3, s17, 11
	s_lshl_b32 s57, s18, 6
	s_add_u32 s3, s3, s57
	s_lshl_b32 s57, s16, 3
	s_add_u32 s3, s3, s57
	s_lshl_b32 s3, s3, 2
	s_add_u32 s28, s28, s3
	s_addc_u32 s29, s29, 0
	v_and_b32_e32 v36, 7, v0
	v_lshlrev_b32_e32 v36, 2, v36
	global_load_dword v37, v36, s[28:29]
	s_lshl_b32 s3, s17, 13
	s_add_u32 s30, s30, s3
	s_addc_u32 s31, s31, 0
	v_lshlrev_b32_e32 v38, 4, v0
	global_load_dwordx4 v[24:27], v38, s[30:31]
	s_add_u32 s3, s19, 0
	s_and_b32 s3, s3, 7
	s_lshl_b32 s57, s3, 10
	s_add_u32 s48, s57, s22
	s_add_u32 s49, s48, 0x2000
	s_add_u32 s50, s48, 0x4000
	s_add_u32 s51, s48, 0x6000
	s_add_u32 s52, s48, 0x8000
	s_add_u32 s53, s48, 0xa000
	s_add_u32 s54, s48, 0xc000
	s_add_u32 s55, s48, 0xe000
	s_lshl_b32 s56, s3, 15
	s_add_u32 s56, s56, s23
	buffer_load_dwordx4 v[88:91], v1, s[4:7], s48 offen nt
	buffer_load_dwordx4 v[92:95], v1, s[4:7], s49 offen nt
	buffer_load_dwordx4 v[96:99], v1, s[4:7], s50 offen nt
	buffer_load_dwordx4 v[100:103], v1, s[4:7], s51 offen nt
	buffer_load_dwordx4 v[104:107], v1, s[4:7], s52 offen nt
	buffer_load_dwordx4 v[108:111], v1, s[4:7], s53 offen nt
	buffer_load_dwordx4 v[112:115], v1, s[4:7], s54 offen nt
	buffer_load_dwordx4 v[116:119], v1, s[4:7], s55 offen nt
	buffer_load_dwordx4 v[152:155], v1, s[8:11], s56 offen
	buffer_load_dwordx4 v[156:159], v1, s[8:11], s56 offen offset:1024
	buffer_load_dwordx4 v[160:163], v1, s[8:11], s56 offen offset:2048
	buffer_load_dwordx4 v[164:167], v1, s[8:11], s56 offen offset:3072
	s_mul_i32 s3, s16, 0x1080
	v_lshlrev_b32_e32 v3, 3, v2
	v_add_u32_e32 v3, s3, v3
	v_add_u32_e32 v4, 0x840, v3
	v_add_u32_e32 v5, 0x8400, v3
	v_add_u32_e32 v6, 0x8400, v4
	v_and_b32_e32 v36, 31, v2
	v_mul_u32_u24_e32 v36, 0x210, v36
	v_lshrrev_b32_e32 v38, 5, v2
	v_lshlrev_b32_e32 v38, 4, v38
	v_add_u32_e32 v7, v36, v38
	s_mul_i32 s3, s20, 0x4200
	s_lshl_b32 s57, s21, 7
	s_add_u32 s3, s3, s57
	v_add_u32_e32 v7, s3, v7
	s_lshl_b32 s3, s21, 13
	s_add_u32 s3, s3, 0x14800
	v_add_u32_e32 v8, s3, v1
	s_add_u32 s3, s23, 0x14800
	v_add_u32_e32 v9, s3, v1
	v_add_u32_e32 v10, 0x10800, v1
	v_mov_b32_e32 v12, 0x3c003c00
	v_mov_b32_e32 v13, 0x3c003c00
	v_mov_b32_e32 v14, 0x3c003c00
	v_mov_b32_e32 v15, 0x3c003c00
	v_mov_b32_e32 v40, 0
	v_mov_b32_e32 v41, 0
	v_mov_b32_e32 v42, 0
	v_mov_b32_e32 v43, 0
	v_mov_b32_e32 v44, 0
	v_mov_b32_e32 v45, 0
	v_mov_b32_e32 v46, 0
	v_mov_b32_e32 v47, 0
	v_mov_b32_e32 v48, 0
	v_mov_b32_e32 v49, 0
	v_mov_b32_e32 v50, 0
	v_mov_b32_e32 v51, 0
	v_mov_b32_e32 v52, 0
	v_mov_b32_e32 v53, 0
	v_mov_b32_e32 v54, 0
	v_mov_b32_e32 v55, 0
	v_mov_b32_e32 v56, 0
	v_mov_b32_e32 v57, 0
	v_mov_b32_e32 v58, 0
	v_mov_b32_e32 v59, 0
	v_mov_b32_e32 v60, 0
	v_mov_b32_e32 v61, 0
	v_mov_b32_e32 v62, 0
	v_mov_b32_e32 v63, 0
	v_mov_b32_e32 v64, 0
	v_mov_b32_e32 v65, 0
	v_mov_b32_e32 v66, 0
	v_mov_b32_e32 v67, 0
	v_mov_b32_e32 v68, 0
	v_mov_b32_e32 v69, 0
	v_mov_b32_e32 v70, 0
	v_mov_b32_e32 v71, 0
	v_mov_b32_e32 v72, 0
	v_mov_b32_e32 v73, 0
	v_mov_b32_e32 v74, 0
	v_mov_b32_e32 v75, 0
	v_mov_b32_e32 v76, 0
	v_mov_b32_e32 v77, 0
	v_mov_b32_e32 v78, 0
	v_mov_b32_e32 v79, 0
	v_mov_b32_e32 v80, 0
	v_mov_b32_e32 v81, 0
	v_mov_b32_e32 v82, 0
	v_mov_b32_e32 v83, 0
	v_mov_b32_e32 v84, 0
	v_mov_b32_e32 v85, 0
	v_mov_b32_e32 v86, 0
	v_mov_b32_e32 v87, 0
	s_lshl_b32 s3, s17, 11
	s_lshl_b32 s57, s18, 6
	s_add_u32 s3, s3, s57
	s_lshl_b32 s57, s20, 5
	s_add_u32 s3, s3, s57
	s_lshl_b32 s57, s21, 3
	s_add_u32 s3, s3, s57
	s_lshl_b32 s3, s3, 8
	s_add_u32 s12, s12, s3
	s_addc_u32 s13, s13, 0
	s_waitcnt vmcnt(12)
	v_max_f32_e32 v28, v24, v25
	v_max3_f32 v28, v28, v26, v27
	v_lshlrev_b32_e32 v29, 2, v2
	v_xor_b32_e32 v30, 4, v29
	ds_bpermute_b32 v31, v30, v28
	s_waitcnt lgkmcnt(0)
	v_max_f32_e32 v28, v28, v31
	v_xor_b32_e32 v30, 8, v29
	ds_bpermute_b32 v31, v30, v28
	s_waitcnt lgkmcnt(0)
	v_max_f32_e32 v28, v28, v31
	v_xor_b32_e32 v30, 16, v29
	ds_bpermute_b32 v31, v30, v28
	s_waitcnt lgkmcnt(0)
	v_max_f32_e32 v28, v28, v31
	v_xor_b32_e32 v30, 32, v29
	ds_bpermute_b32 v31, v30, v28
	s_waitcnt lgkmcnt(0)
	v_max_f32_e32 v28, v28, v31
	v_xor_b32_e32 v30, 64, v29
	ds_bpermute_b32 v31, v30, v28
	s_waitcnt lgkmcnt(0)
	v_max_f32_e32 v28, v28, v31
	v_xor_b32_e32 v30, 128, v29
	ds_bpermute_b32 v31, v30, v28
	s_waitcnt lgkmcnt(0)
	v_max_f32_e32 v28, v28, v31
	s_lshl_b32 s3, s16, 2
	s_add_u32 s3, s3, 0x24800
	v_mov_b32_e32 v30, s3
	ds_write_b32 v30, v28
	s_waitcnt lgkmcnt(0)
	s_barrier
	v_mov_b32_e32 v30, 0x24800
	ds_read_b128 v[32:35], v30
	ds_read_b128 v[16:19], v30 offset:16
	s_waitcnt lgkmcnt(0)
	v_max3_f32 v28, v32, v33, v34
	v_max3_f32 v28, v28, v35, v16
	v_max3_f32 v28, v28, v17, v18
	v_max_f32_e32 v28, v28, v19
	v_sub_f32_e32 v16, v24, v28
	v_sub_f32_e32 v17, v25, v28
	v_sub_f32_e32 v18, v26, v28
	v_sub_f32_e32 v19, v27, v28
	v_mul_f32_e32 v20, 0x3e4ccccd, v16
	v_mul_f32_e32 v21, 0x3e4ccccd, v17
	v_mul_f32_e32 v22, 0x3e4ccccd, v18
	v_mul_f32_e32 v23, 0x3e4ccccd, v19
	v_exp_f32_e32 v16, v16
	v_exp_f32_e32 v17, v17
	v_exp_f32_e32 v18, v18
	v_exp_f32_e32 v19, v19
	v_exp_f32_e32 v20, v20
	v_exp_f32_e32 v21, v21
	v_exp_f32_e32 v22, v22
	v_exp_f32_e32 v23, v23
	v_lshlrev_b32_e32 v30, 4, v0
	v_add_u32_e32 v30, 0x10800, v30
	ds_write_b128 v30, v[16:19]
	ds_write_b128 v30, v[20:23] offset:8192
	v_add_f32_e32 v36, v37, v28
	v_mul_f32_e32 v38, 0x3e4ccccd, v36
	v_max_f32_e32 v39, v36, v38
	v_sub_f32_e32 v36, v36, v39
	v_sub_f32_e32 v38, v38, v39
	v_add_f32_e32 v36, 0x41600000, v36
	v_add_f32_e32 v38, 0x41600000, v38
	v_exp_f32_e32 v36, v36
	v_exp_f32_e32 v38, v38
	s_nop 1
	v_readlane_b32 s32, v36, 0
	v_readlane_b32 s33, v36, 1
	v_readlane_b32 s34, v36, 2
	v_readlane_b32 s35, v36, 3
	v_readlane_b32 s36, v36, 4
	v_readlane_b32 s37, v36, 5
	v_readlane_b32 s38, v36, 6
	v_readlane_b32 s39, v36, 7
	v_readlane_b32 s40, v38, 0
	v_readlane_b32 s41, v38, 1
	v_readlane_b32 s42, v38, 2
	v_readlane_b32 s43, v38, 3
	v_readlane_b32 s44, v38, 4
	v_readlane_b32 s45, v38, 5
	v_readlane_b32 s46, v38, 6
	v_readlane_b32 s47, v38, 7
	s_waitcnt lgkmcnt(0)
	s_barrier
	s_lshl_b32 s3, s19, 10
	v_add_u32_e32 v11, s3, v10
	ds_read_b128 v[16:19], v11
	ds_read_b128 v[20:23], v11 offset:8192
	s_waitcnt lgkmcnt(0)
	s_add_u32 s3, s19, 1
	s_and_b32 s3, s3, 7
	s_lshl_b32 s57, s3, 10
	s_add_u32 s48, s57, s22
	s_add_u32 s49, s48, 0x2000
	s_add_u32 s50, s48, 0x4000
	s_add_u32 s51, s48, 0x6000
	s_add_u32 s52, s48, 0x8000
	s_add_u32 s53, s48, 0xa000
	s_add_u32 s54, s48, 0xc000
	s_add_u32 s55, s48, 0xe000
	s_lshl_b32 s56, s3, 15
	s_add_u32 s56, s56, s23
	buffer_load_dwordx4 v[120:123], v1, s[4:7], s48 offen nt
	buffer_load_dwordx4 v[124:127], v1, s[4:7], s49 offen nt
	buffer_load_dwordx4 v[128:131], v1, s[4:7], s50 offen nt
	buffer_load_dwordx4 v[132:135], v1, s[4:7], s51 offen nt
	buffer_load_dwordx4 v[136:139], v1, s[4:7], s52 offen nt
	buffer_load_dwordx4 v[140:143], v1, s[4:7], s53 offen nt
	buffer_load_dwordx4 v[144:147], v1, s[4:7], s54 offen nt
	buffer_load_dwordx4 v[148:151], v1, s[4:7], s55 offen nt
	buffer_load_dwordx4 v[168:171], v1, s[8:11], s56 offen
	buffer_load_dwordx4 v[172:175], v1, s[8:11], s56 offen offset:1024
	buffer_load_dwordx4 v[176:179], v1, s[8:11], s56 offen offset:2048
	buffer_load_dwordx4 v[180:183], v1, s[8:11], s56 offen offset:3072
	s_waitcnt vmcnt(23)
	v_pk_mul_f32 v[24:25], v[16:17], s[32:33] op_sel_hi:[1,0]
	v_pk_mul_f32 v[26:27], v[18:19], s[32:33] op_sel_hi:[1,0]
	v_pk_mul_f32 v[28:29], v[20:21], s[40:41] op_sel_hi:[1,0]
	v_pk_mul_f32 v[30:31], v[22:23], s[40:41] op_sel_hi:[1,0]
	v_cmp_lt_i32_e64 s[60:61], 0, v88
	v_cmp_lt_i32_e64 s[62:63], 0, v89
	v_cmp_lt_i32_e64 s[64:65], 0, v90
	v_cmp_lt_i32_e64 s[66:67], 0, v91
	v_max_f32_e32 v24, v24, v28
	v_max_f32_e32 v25, v25, v29
	v_max_f32_e32 v26, v26, v30
	v_max_f32_e32 v27, v27, v31
	v_cndmask_b32_e64 v24, 0, v24, s[60:61]
	v_cndmask_b32_e64 v25, 0, v25, s[62:63]
	v_cndmask_b32_e64 v26, 0, v26, s[64:65]
	v_cndmask_b32_e64 v27, 0, v27, s[66:67]
	v_cvt_pkrtz_f16_f32 v32, v24, v25
	v_cvt_pkrtz_f16_f32 v33, v26, v27
	s_waitcnt vmcnt(22)
	v_pk_mul_f32 v[24:25], v[16:17], s[32:33] op_sel:[0,1] op_sel_hi:[1,1]
	v_pk_mul_f32 v[26:27], v[18:19], s[32:33] op_sel:[0,1] op_sel_hi:[1,1]
	v_pk_mul_f32 v[28:29], v[20:21], s[40:41] op_sel:[0,1] op_sel_hi:[1,1]
	v_pk_mul_f32 v[30:31], v[22:23], s[40:41] op_sel:[0,1] op_sel_hi:[1,1]
	v_cmp_lt_i32_e64 s[60:61], 0, v92
	v_cmp_lt_i32_e64 s[62:63], 0, v93
	v_cmp_lt_i32_e64 s[64:65], 0, v94
	v_cmp_lt_i32_e64 s[66:67], 0, v95
	v_max_f32_e32 v24, v24, v28
	v_max_f32_e32 v25, v25, v29
	v_max_f32_e32 v26, v26, v30
	v_max_f32_e32 v27, v27, v31
	v_cndmask_b32_e64 v24, 0, v24, s[60:61]
	v_cndmask_b32_e64 v25, 0, v25, s[62:63]
	v_cndmask_b32_e64 v26, 0, v26, s[64:65]
	v_cndmask_b32_e64 v27, 0, v27, s[66:67]
	v_cvt_pkrtz_f16_f32 v34, v24, v25
	v_cvt_pkrtz_f16_f32 v35, v26, v27
	ds_write2_b64 v3, v[32:33], v[34:35] offset0:0 offset1:66
	s_waitcnt vmcnt(21)
	v_pk_mul_f32 v[24:25], v[16:17], s[34:35] op_sel_hi:[1,0]
	v_pk_mul_f32 v[26:27], v[18:19], s[34:35] op_sel_hi:[1,0]
	v_pk_mul_f32 v[28:29], v[20:21], s[42:43] op_sel_hi:[1,0]
	v_pk_mul_f32 v[30:31], v[22:23], s[42:43] op_sel_hi:[1,0]
	v_cmp_lt_i32_e64 s[60:61], 0, v96
	v_cmp_lt_i32_e64 s[62:63], 0, v97
	v_cmp_lt_i32_e64 s[64:65], 0, v98
	v_cmp_lt_i32_e64 s[66:67], 0, v99
	v_max_f32_e32 v24, v24, v28
	v_max_f32_e32 v25, v25, v29
	v_max_f32_e32 v26, v26, v30
	v_max_f32_e32 v27, v27, v31
	v_cndmask_b32_e64 v24, 0, v24, s[60:61]
	v_cndmask_b32_e64 v25, 0, v25, s[62:63]
	v_cndmask_b32_e64 v26, 0, v26, s[64:65]
	v_cndmask_b32_e64 v27, 0, v27, s[66:67]
	v_cvt_pkrtz_f16_f32 v32, v24, v25
	v_cvt_pkrtz_f16_f32 v33, v26, v27
	s_waitcnt vmcnt(20)
	v_pk_mul_f32 v[24:25], v[16:17], s[34:35] op_sel:[0,1] op_sel_hi:[1,1]
	v_pk_mul_f32 v[26:27], v[18:19], s[34:35] op_sel:[0,1] op_sel_hi:[1,1]
	v_pk_mul_f32 v[28:29], v[20:21], s[42:43] op_sel:[0,1] op_sel_hi:[1,1]
	v_pk_mul_f32 v[30:31], v[22:23], s[42:43] op_sel:[0,1] op_sel_hi:[1,1]
	v_cmp_lt_i32_e64 s[60:61], 0, v100
	v_cmp_lt_i32_e64 s[62:63], 0, v101
	v_cmp_lt_i32_e64 s[64:65], 0, v102
	v_cmp_lt_i32_e64 s[66:67], 0, v103
	v_max_f32_e32 v24, v24, v28
	v_max_f32_e32 v25, v25, v29
	v_max_f32_e32 v26, v26, v30
	v_max_f32_e32 v27, v27, v31
	v_cndmask_b32_e64 v24, 0, v24, s[60:61]
	v_cndmask_b32_e64 v25, 0, v25, s[62:63]
	v_cndmask_b32_e64 v26, 0, v26, s[64:65]
	v_cndmask_b32_e64 v27, 0, v27, s[66:67]
	v_cvt_pkrtz_f16_f32 v34, v24, v25
	v_cvt_pkrtz_f16_f32 v35, v26, v27
	ds_write2_b64 v3, v[32:33], v[34:35] offset0:132 offset1:198
	s_waitcnt vmcnt(19)
	v_pk_mul_f32 v[24:25], v[16:17], s[36:37] op_sel_hi:[1,0]
	v_pk_mul_f32 v[26:27], v[18:19], s[36:37] op_sel_hi:[1,0]
	v_pk_mul_f32 v[28:29], v[20:21], s[44:45] op_sel_hi:[1,0]
	v_pk_mul_f32 v[30:31], v[22:23], s[44:45] op_sel_hi:[1,0]
	v_cmp_lt_i32_e64 s[60:61], 0, v104
	v_cmp_lt_i32_e64 s[62:63], 0, v105
	v_cmp_lt_i32_e64 s[64:65], 0, v106
	v_cmp_lt_i32_e64 s[66:67], 0, v107
	v_max_f32_e32 v24, v24, v28
	v_max_f32_e32 v25, v25, v29
	v_max_f32_e32 v26, v26, v30
	v_max_f32_e32 v27, v27, v31
	v_cndmask_b32_e64 v24, 0, v24, s[60:61]
	v_cndmask_b32_e64 v25, 0, v25, s[62:63]
	v_cndmask_b32_e64 v26, 0, v26, s[64:65]
	v_cndmask_b32_e64 v27, 0, v27, s[66:67]
	v_cvt_pkrtz_f16_f32 v32, v24, v25
	v_cvt_pkrtz_f16_f32 v33, v26, v27
	s_waitcnt vmcnt(18)
	v_pk_mul_f32 v[24:25], v[16:17], s[36:37] op_sel:[0,1] op_sel_hi:[1,1]
	v_pk_mul_f32 v[26:27], v[18:19], s[36:37] op_sel:[0,1] op_sel_hi:[1,1]
	v_pk_mul_f32 v[28:29], v[20:21], s[44:45] op_sel:[0,1] op_sel_hi:[1,1]
	v_pk_mul_f32 v[30:31], v[22:23], s[44:45] op_sel:[0,1] op_sel_hi:[1,1]
	v_cmp_lt_i32_e64 s[60:61], 0, v108
	v_cmp_lt_i32_e64 s[62:63], 0, v109
	v_cmp_lt_i32_e64 s[64:65], 0, v110
	v_cmp_lt_i32_e64 s[66:67], 0, v111
	v_max_f32_e32 v24, v24, v28
	v_max_f32_e32 v25, v25, v29
	v_max_f32_e32 v26, v26, v30
	v_max_f32_e32 v27, v27, v31
	v_cndmask_b32_e64 v24, 0, v24, s[60:61]
	v_cndmask_b32_e64 v25, 0, v25, s[62:63]
	v_cndmask_b32_e64 v26, 0, v26, s[64:65]
	v_cndmask_b32_e64 v27, 0, v27, s[66:67]
	v_cvt_pkrtz_f16_f32 v34, v24, v25
	v_cvt_pkrtz_f16_f32 v35, v26, v27
	ds_write2_b64 v4, v[32:33], v[34:35] offset0:0 offset1:66
	s_waitcnt vmcnt(17)
	v_pk_mul_f32 v[24:25], v[16:17], s[38:39] op_sel_hi:[1,0]
	v_pk_mul_f32 v[26:27], v[18:19], s[38:39] op_sel_hi:[1,0]
	v_pk_mul_f32 v[28:29], v[20:21], s[46:47] op_sel_hi:[1,0]
	v_pk_mul_f32 v[30:31], v[22:23], s[46:47] op_sel_hi:[1,0]
	v_cmp_lt_i32_e64 s[60:61], 0, v112
	v_cmp_lt_i32_e64 s[62:63], 0, v113
	v_cmp_lt_i32_e64 s[64:65], 0, v114
	v_cmp_lt_i32_e64 s[66:67], 0, v115
	v_max_f32_e32 v24, v24, v28
	v_max_f32_e32 v25, v25, v29
	v_max_f32_e32 v26, v26, v30
	v_max_f32_e32 v27, v27, v31
	v_cndmask_b32_e64 v24, 0, v24, s[60:61]
	v_cndmask_b32_e64 v25, 0, v25, s[62:63]
	v_cndmask_b32_e64 v26, 0, v26, s[64:65]
	v_cndmask_b32_e64 v27, 0, v27, s[66:67]
	v_cvt_pkrtz_f16_f32 v32, v24, v25
	v_cvt_pkrtz_f16_f32 v33, v26, v27
	s_waitcnt vmcnt(16)
	v_pk_mul_f32 v[24:25], v[16:17], s[38:39] op_sel:[0,1] op_sel_hi:[1,1]
	v_pk_mul_f32 v[26:27], v[18:19], s[38:39] op_sel:[0,1] op_sel_hi:[1,1]
	v_pk_mul_f32 v[28:29], v[20:21], s[46:47] op_sel:[0,1] op_sel_hi:[1,1]
	v_pk_mul_f32 v[30:31], v[22:23], s[46:47] op_sel:[0,1] op_sel_hi:[1,1]
	v_cmp_lt_i32_e64 s[60:61], 0, v116
	v_cmp_lt_i32_e64 s[62:63], 0, v117
	v_cmp_lt_i32_e64 s[64:65], 0, v118
	v_cmp_lt_i32_e64 s[66:67], 0, v119
	v_max_f32_e32 v24, v24, v28
	v_max_f32_e32 v25, v25, v29
	v_max_f32_e32 v26, v26, v30
	v_max_f32_e32 v27, v27, v31
	v_cndmask_b32_e64 v24, 0, v24, s[60:61]
	v_cndmask_b32_e64 v25, 0, v25, s[62:63]
	v_cndmask_b32_e64 v26, 0, v26, s[64:65]
	v_cndmask_b32_e64 v27, 0, v27, s[66:67]
	v_cvt_pkrtz_f16_f32 v34, v24, v25
	v_cvt_pkrtz_f16_f32 v35, v26, v27
	ds_write2_b64 v4, v[32:33], v[34:35] offset0:132 offset1:198
	s_waitcnt vmcnt(12)
	ds_write_b128 v9, v[152:155] offset:0
	ds_write_b128 v9, v[156:159] offset:1024
	ds_write_b128 v9, v[160:163] offset:2048
	ds_write_b128 v9, v[164:167] offset:3072
	s_add_u32 s3, s19, 1
	s_and_b32 s3, s3, 7
	s_lshl_b32 s3, s3, 10
	v_add_u32_e32 v11, s3, v10
	ds_read_b128 v[16:19], v11
	ds_read_b128 v[20:23], v11 offset:8192
	s_waitcnt lgkmcnt(0)
	s_barrier
	ds_read_b128 v[184:187], v7 offset:0
	ds_read_b128 v[200:203], v8 offset:0
	ds_read_b128 v[204:207], v8 offset:1024
	ds_read_b128 v[188:191], v7 offset:32
	ds_read_b128 v[208:211], v8 offset:2048
	ds_read_b128 v[212:215], v8 offset:3072
	ds_read_b128 v[192:195], v7 offset:64
	ds_read_b128 v[216:219], v8 offset:4096
	ds_read_b128 v[220:223], v8 offset:5120
	ds_read_b128 v[196:199], v7 offset:96
	ds_read_b128 v[224:227], v8 offset:6144
	ds_read_b128 v[228:231], v8 offset:7168
	s_add_u32 s3, s19, 2
	s_and_b32 s3, s3, 7
	s_lshl_b32 s57, s3, 10
	s_add_u32 s48, s57, s22
	s_add_u32 s49, s48, 0x2000
	s_add_u32 s50, s48, 0x4000
	s_add_u32 s51, s48, 0x6000
	s_add_u32 s52, s48, 0x8000
	s_add_u32 s53, s48, 0xa000
	s_add_u32 s54, s48, 0xc000
	s_add_u32 s55, s48, 0xe000
	s_lshl_b32 s56, s3, 15
	s_add_u32 s56, s56, s23
	buffer_load_dwordx4 v[88:91], v1, s[4:7], s48 offen nt
	buffer_load_dwordx4 v[92:95], v1, s[4:7], s49 offen nt
	buffer_load_dwordx4 v[96:99], v1, s[4:7], s50 offen nt
	buffer_load_dwordx4 v[100:103], v1, s[4:7], s51 offen nt
	buffer_load_dwordx4 v[104:107], v1, s[4:7], s52 offen nt
	buffer_load_dwordx4 v[108:111], v1, s[4:7], s53 offen nt
	buffer_load_dwordx4 v[112:115], v1, s[4:7], s54 offen nt
	buffer_load_dwordx4 v[116:119], v1, s[4:7], s55 offen nt
	buffer_load_dwordx4 v[152:155], v1, s[8:11], s56 offen
	buffer_load_dwordx4 v[156:159], v1, s[8:11], s56 offen offset:1024
	buffer_load_dwordx4 v[160:163], v1, s[8:11], s56 offen offset:2048
	buffer_load_dwordx4 v[164:167], v1, s[8:11], s56 offen offset:3072
	s_waitcnt vmcnt(23)
	v_pk_mul_f32 v[24:25], v[16:17], s[32:33] op_sel_hi:[1,0]
	v_pk_mul_f32 v[26:27], v[18:19], s[32:33] op_sel_hi:[1,0]
	v_pk_mul_f32 v[28:29], v[20:21], s[40:41] op_sel_hi:[1,0]
	v_pk_mul_f32 v[30:31], v[22:23], s[40:41] op_sel_hi:[1,0]
	v_cmp_lt_i32_e64 s[60:61], 0, v120
	v_cmp_lt_i32_e64 s[62:63], 0, v121
	v_cmp_lt_i32_e64 s[64:65], 0, v122
	v_cmp_lt_i32_e64 s[66:67], 0, v123
	v_max_f32_e32 v24, v24, v28
	v_max_f32_e32 v25, v25, v29
	v_max_f32_e32 v26, v26, v30
	v_max_f32_e32 v27, v27, v31
	v_cndmask_b32_e64 v24, 0, v24, s[60:61]
	v_cndmask_b32_e64 v25, 0, v25, s[62:63]
	v_cndmask_b32_e64 v26, 0, v26, s[64:65]
	v_cndmask_b32_e64 v27, 0, v27, s[66:67]
	v_cvt_pkrtz_f16_f32 v32, v24, v25
	v_cvt_pkrtz_f16_f32 v33, v26, v27
	s_waitcnt vmcnt(22)
	s_waitcnt lgkmcnt(0)
	v_pk_mul_f32 v[24:25], v[16:17], s[32:33] op_sel:[0,1] op_sel_hi:[1,1]
	v_pk_mul_f32 v[26:27], v[18:19], s[32:33] op_sel:[0,1] op_sel_hi:[1,1]
	v_pk_mul_f32 v[28:29], v[20:21], s[40:41] op_sel:[0,1] op_sel_hi:[1,1]
	v_pk_mul_f32 v[30:31], v[22:23], s[40:41] op_sel:[0,1] op_sel_hi:[1,1]
	v_mfma_f32_32x32x16_f16 v[40:55], v[184:187], v[200:203], v[40:55]
	v_cmp_lt_i32_e64 s[60:61], 0, v124
	v_cmp_lt_i32_e64 s[62:63], 0, v125
	v_cmp_lt_i32_e64 s[64:65], 0, v126
	v_cmp_lt_i32_e64 s[66:67], 0, v127
	v_max_f32_e32 v24, v24, v28
	v_max_f32_e32 v25, v25, v29
	v_max_f32_e32 v26, v26, v30
	v_max_f32_e32 v27, v27, v31
	v_cndmask_b32_e64 v24, 0, v24, s[60:61]
	v_cndmask_b32_e64 v25, 0, v25, s[62:63]
	v_cndmask_b32_e64 v26, 0, v26, s[64:65]
	v_cndmask_b32_e64 v27, 0, v27, s[66:67]
	v_mfma_f32_32x32x16_f16 v[56:71], v[184:187], v[204:207], v[56:71]
	v_cvt_pkrtz_f16_f32 v34, v24, v25
	v_cvt_pkrtz_f16_f32 v35, v26, v27
	ds_write2_b64 v5, v[32:33], v[34:35] offset0:0 offset1:66
	s_waitcnt vmcnt(21)
	v_pk_mul_f32 v[24:25], v[16:17], s[34:35] op_sel_hi:[1,0]
	v_pk_mul_f32 v[26:27], v[18:19], s[34:35] op_sel_hi:[1,0]
	v_pk_mul_f32 v[28:29], v[20:21], s[42:43] op_sel_hi:[1,0]
	v_pk_mul_f32 v[30:31], v[22:23], s[42:43] op_sel_hi:[1,0]
	v_mfma_f32_32x32x16_f16 v[72:87], v[184:187], v[12:15], v[72:87]
	v_cmp_lt_i32_e64 s[60:61], 0, v128
	v_cmp_lt_i32_e64 s[62:63], 0, v129
	v_cmp_lt_i32_e64 s[64:65], 0, v130
	v_cmp_lt_i32_e64 s[66:67], 0, v131
	v_max_f32_e32 v24, v24, v28
	v_max_f32_e32 v25, v25, v29
	v_max_f32_e32 v26, v26, v30
	v_max_f32_e32 v27, v27, v31
	v_cndmask_b32_e64 v24, 0, v24, s[60:61]
	v_cndmask_b32_e64 v25, 0, v25, s[62:63]
	v_cndmask_b32_e64 v26, 0, v26, s[64:65]
	v_cndmask_b32_e64 v27, 0, v27, s[66:67]
	v_mfma_f32_32x32x16_f16 v[40:55], v[188:191], v[208:211], v[40:55]
	v_cvt_pkrtz_f16_f32 v32, v24, v25
	v_cvt_pkrtz_f16_f32 v33, v26, v27
	s_waitcnt vmcnt(20)
	v_pk_mul_f32 v[24:25], v[16:17], s[34:35] op_sel:[0,1] op_sel_hi:[1,1]
	v_pk_mul_f32 v[26:27], v[18:19], s[34:35] op_sel:[0,1] op_sel_hi:[1,1]
	v_pk_mul_f32 v[28:29], v[20:21], s[42:43] op_sel:[0,1] op_sel_hi:[1,1]
	v_pk_mul_f32 v[30:31], v[22:23], s[42:43] op_sel:[0,1] op_sel_hi:[1,1]
	v_mfma_f32_32x32x16_f16 v[56:71], v[188:191], v[212:215], v[56:71]
	v_cmp_lt_i32_e64 s[60:61], 0, v132
	v_cmp_lt_i32_e64 s[62:63], 0, v133
	v_cmp_lt_i32_e64 s[64:65], 0, v134
	v_cmp_lt_i32_e64 s[66:67], 0, v135
	v_max_f32_e32 v24, v24, v28
	v_max_f32_e32 v25, v25, v29
	v_max_f32_e32 v26, v26, v30
	v_max_f32_e32 v27, v27, v31
	v_cndmask_b32_e64 v24, 0, v24, s[60:61]
	v_cndmask_b32_e64 v25, 0, v25, s[62:63]
	v_cndmask_b32_e64 v26, 0, v26, s[64:65]
	v_cndmask_b32_e64 v27, 0, v27, s[66:67]
	v_mfma_f32_32x32x16_f16 v[72:87], v[188:191], v[12:15], v[72:87]
	v_cvt_pkrtz_f16_f32 v34, v24, v25
	v_cvt_pkrtz_f16_f32 v35, v26, v27
	ds_write2_b64 v5, v[32:33], v[34:35] offset0:132 offset1:198
	s_waitcnt vmcnt(19)
	v_pk_mul_f32 v[24:25], v[16:17], s[36:37] op_sel_hi:[1,0]
	v_pk_mul_f32 v[26:27], v[18:19], s[36:37] op_sel_hi:[1,0]
	v_pk_mul_f32 v[28:29], v[20:21], s[44:45] op_sel_hi:[1,0]
	v_pk_mul_f32 v[30:31], v[22:23], s[44:45] op_sel_hi:[1,0]
	v_mfma_f32_32x32x16_f16 v[40:55], v[192:195], v[216:219], v[40:55]
	v_cmp_lt_i32_e64 s[60:61], 0, v136
	v_cmp_lt_i32_e64 s[62:63], 0, v137
	v_cmp_lt_i32_e64 s[64:65], 0, v138
	v_cmp_lt_i32_e64 s[66:67], 0, v139
	v_max_f32_e32 v24, v24, v28
	v_max_f32_e32 v25, v25, v29
	v_max_f32_e32 v26, v26, v30
	v_max_f32_e32 v27, v27, v31
	v_cndmask_b32_e64 v24, 0, v24, s[60:61]
	v_cndmask_b32_e64 v25, 0, v25, s[62:63]
	v_cndmask_b32_e64 v26, 0, v26, s[64:65]
	v_cndmask_b32_e64 v27, 0, v27, s[66:67]
	v_mfma_f32_32x32x16_f16 v[56:71], v[192:195], v[220:223], v[56:71]
	v_cvt_pkrtz_f16_f32 v32, v24, v25
	v_cvt_pkrtz_f16_f32 v33, v26, v27
	s_waitcnt vmcnt(18)
	v_pk_mul_f32 v[24:25], v[16:17], s[36:37] op_sel:[0,1] op_sel_hi:[1,1]
	v_pk_mul_f32 v[26:27], v[18:19], s[36:37] op_sel:[0,1] op_sel_hi:[1,1]
	v_pk_mul_f32 v[28:29], v[20:21], s[44:45] op_sel:[0,1] op_sel_hi:[1,1]
	v_pk_mul_f32 v[30:31], v[22:23], s[44:45] op_sel:[0,1] op_sel_hi:[1,1]
	v_mfma_f32_32x32x16_f16 v[72:87], v[192:195], v[12:15], v[72:87]
	v_cmp_lt_i32_e64 s[60:61], 0, v140
	v_cmp_lt_i32_e64 s[62:63], 0, v141
	v_cmp_lt_i32_e64 s[64:65], 0, v142
	v_cmp_lt_i32_e64 s[66:67], 0, v143
	v_max_f32_e32 v24, v24, v28
	v_max_f32_e32 v25, v25, v29
	v_max_f32_e32 v26, v26, v30
	v_max_f32_e32 v27, v27, v31
	v_cndmask_b32_e64 v24, 0, v24, s[60:61]
	v_cndmask_b32_e64 v25, 0, v25, s[62:63]
	v_cndmask_b32_e64 v26, 0, v26, s[64:65]
	v_cndmask_b32_e64 v27, 0, v27, s[66:67]
	v_mfma_f32_32x32x16_f16 v[40:55], v[196:199], v[224:227], v[40:55]
	v_cvt_pkrtz_f16_f32 v34, v24, v25
	v_cvt_pkrtz_f16_f32 v35, v26, v27
	ds_write2_b64 v6, v[32:33], v[34:35] offset0:0 offset1:66
	s_waitcnt vmcnt(17)
	v_pk_mul_f32 v[24:25], v[16:17], s[38:39] op_sel_hi:[1,0]
	v_pk_mul_f32 v[26:27], v[18:19], s[38:39] op_sel_hi:[1,0]
	v_pk_mul_f32 v[28:29], v[20:21], s[46:47] op_sel_hi:[1,0]
	v_pk_mul_f32 v[30:31], v[22:23], s[46:47] op_sel_hi:[1,0]
	v_mfma_f32_32x32x16_f16 v[56:71], v[196:199], v[228:231], v[56:71]
	v_cmp_lt_i32_e64 s[60:61], 0, v144
	v_cmp_lt_i32_e64 s[62:63], 0, v145
	v_cmp_lt_i32_e64 s[64:65], 0, v146
	v_cmp_lt_i32_e64 s[66:67], 0, v147
	v_max_f32_e32 v24, v24, v28
	v_max_f32_e32 v25, v25, v29
	v_max_f32_e32 v26, v26, v30
	v_max_f32_e32 v27, v27, v31
	v_cndmask_b32_e64 v24, 0, v24, s[60:61]
	v_cndmask_b32_e64 v25, 0, v25, s[62:63]
	v_cndmask_b32_e64 v26, 0, v26, s[64:65]
	v_cndmask_b32_e64 v27, 0, v27, s[66:67]
	v_cvt_pkrtz_f16_f32 v32, v24, v25
	v_cvt_pkrtz_f16_f32 v33, v26, v27
	s_waitcnt vmcnt(16)
	v_pk_mul_f32 v[24:25], v[16:17], s[38:39] op_sel:[0,1] op_sel_hi:[1,1]
	v_pk_mul_f32 v[26:27], v[18:19], s[38:39] op_sel:[0,1] op_sel_hi:[1,1]
	v_pk_mul_f32 v[28:29], v[20:21], s[46:47] op_sel:[0,1] op_sel_hi:[1,1]
	v_pk_mul_f32 v[30:31], v[22:23], s[46:47] op_sel:[0,1] op_sel_hi:[1,1]
	v_mfma_f32_32x32x16_f16 v[72:87], v[196:199], v[12:15], v[72:87]
	v_cmp_lt_i32_e64 s[60:61], 0, v148
	v_cmp_lt_i32_e64 s[62:63], 0, v149
	v_cmp_lt_i32_e64 s[64:65], 0, v150
	v_cmp_lt_i32_e64 s[66:67], 0, v151
	v_max_f32_e32 v24, v24, v28
	v_max_f32_e32 v25, v25, v29
	v_max_f32_e32 v26, v26, v30
	v_max_f32_e32 v27, v27, v31
	v_cndmask_b32_e64 v24, 0, v24, s[60:61]
	v_cndmask_b32_e64 v25, 0, v25, s[62:63]
	v_cndmask_b32_e64 v26, 0, v26, s[64:65]
	v_cndmask_b32_e64 v27, 0, v27, s[66:67]
	v_cvt_pkrtz_f16_f32 v34, v24, v25
	v_cvt_pkrtz_f16_f32 v35, v26, v27
	ds_write2_b64 v6, v[32:33], v[34:35] offset0:132 offset1:198
	s_waitcnt vmcnt(12)
	ds_write_b128 v9, v[168:171] offset:32768
	ds_write_b128 v9, v[172:175] offset:33792
	ds_write_b128 v9, v[176:179] offset:34816
	ds_write_b128 v9, v[180:183] offset:35840
	s_add_u32 s3, s19, 2
	s_and_b32 s3, s3, 7
	s_lshl_b32 s3, s3, 10
	v_add_u32_e32 v11, s3, v10
	ds_read_b128 v[16:19], v11
	ds_read_b128 v[20:23], v11 offset:8192
	s_waitcnt lgkmcnt(0)
	s_barrier
	ds_read_b128 v[184:187], v7 offset:33792
	ds_read_b128 v[200:203], v8 offset:32768
	ds_read_b128 v[204:207], v8 offset:33792
	ds_read_b128 v[188:191], v7 offset:33824
	ds_read_b128 v[208:211], v8 offset:34816
	ds_read_b128 v[212:215], v8 offset:35840
	ds_read_b128 v[192:195], v7 offset:33856
	ds_read_b128 v[216:219], v8 offset:36864
	ds_read_b128 v[220:223], v8 offset:37888
	ds_read_b128 v[196:199], v7 offset:33888
	ds_read_b128 v[224:227], v8 offset:38912
	ds_read_b128 v[228:231], v8 offset:39936
	s_add_u32 s3, s19, 3
	s_and_b32 s3, s3, 7
	s_lshl_b32 s57, s3, 10
	s_add_u32 s48, s57, s22
	s_add_u32 s49, s48, 0x2000
	s_add_u32 s50, s48, 0x4000
	s_add_u32 s51, s48, 0x6000
	s_add_u32 s52, s48, 0x8000
	s_add_u32 s53, s48, 0xa000
	s_add_u32 s54, s48, 0xc000
	s_add_u32 s55, s48, 0xe000
	s_lshl_b32 s56, s3, 15
	s_add_u32 s56, s56, s23
	buffer_load_dwordx4 v[120:123], v1, s[4:7], s48 offen nt
	buffer_load_dwordx4 v[124:127], v1, s[4:7], s49 offen nt
	buffer_load_dwordx4 v[128:131], v1, s[4:7], s50 offen nt
	buffer_load_dwordx4 v[132:135], v1, s[4:7], s51 offen nt
	buffer_load_dwordx4 v[136:139], v1, s[4:7], s52 offen nt
	buffer_load_dwordx4 v[140:143], v1, s[4:7], s53 offen nt
	buffer_load_dwordx4 v[144:147], v1, s[4:7], s54 offen nt
	buffer_load_dwordx4 v[148:151], v1, s[4:7], s55 offen nt
	buffer_load_dwordx4 v[168:171], v1, s[8:11], s56 offen
	buffer_load_dwordx4 v[172:175], v1, s[8:11], s56 offen offset:1024
	buffer_load_dwordx4 v[176:179], v1, s[8:11], s56 offen offset:2048
	buffer_load_dwordx4 v[180:183], v1, s[8:11], s56 offen offset:3072
	s_waitcnt vmcnt(23)
	v_pk_mul_f32 v[24:25], v[16:17], s[32:33] op_sel_hi:[1,0]
	v_pk_mul_f32 v[26:27], v[18:19], s[32:33] op_sel_hi:[1,0]
	v_pk_mul_f32 v[28:29], v[20:21], s[40:41] op_sel_hi:[1,0]
	v_pk_mul_f32 v[30:31], v[22:23], s[40:41] op_sel_hi:[1,0]
	v_cmp_lt_i32_e64 s[60:61], 0, v88
	v_cmp_lt_i32_e64 s[62:63], 0, v89
	v_cmp_lt_i32_e64 s[64:65], 0, v90
	v_cmp_lt_i32_e64 s[66:67], 0, v91
	v_max_f32_e32 v24, v24, v28
	v_max_f32_e32 v25, v25, v29
	v_max_f32_e32 v26, v26, v30
	v_max_f32_e32 v27, v27, v31
	v_cndmask_b32_e64 v24, 0, v24, s[60:61]
	v_cndmask_b32_e64 v25, 0, v25, s[62:63]
	v_cndmask_b32_e64 v26, 0, v26, s[64:65]
	v_cndmask_b32_e64 v27, 0, v27, s[66:67]
	v_cvt_pkrtz_f16_f32 v32, v24, v25
	v_cvt_pkrtz_f16_f32 v33, v26, v27
	s_waitcnt vmcnt(22)
	s_waitcnt lgkmcnt(0)
	v_pk_mul_f32 v[24:25], v[16:17], s[32:33] op_sel:[0,1] op_sel_hi:[1,1]
	v_pk_mul_f32 v[26:27], v[18:19], s[32:33] op_sel:[0,1] op_sel_hi:[1,1]
	v_pk_mul_f32 v[28:29], v[20:21], s[40:41] op_sel:[0,1] op_sel_hi:[1,1]
	v_pk_mul_f32 v[30:31], v[22:23], s[40:41] op_sel:[0,1] op_sel_hi:[1,1]
	v_mfma_f32_32x32x16_f16 v[40:55], v[184:187], v[200:203], v[40:55]
	v_cmp_lt_i32_e64 s[60:61], 0, v92
	v_cmp_lt_i32_e64 s[62:63], 0, v93
	v_cmp_lt_i32_e64 s[64:65], 0, v94
	v_cmp_lt_i32_e64 s[66:67], 0, v95
	v_max_f32_e32 v24, v24, v28
	v_max_f32_e32 v25, v25, v29
	v_max_f32_e32 v26, v26, v30
	v_max_f32_e32 v27, v27, v31
	v_cndmask_b32_e64 v24, 0, v24, s[60:61]
	v_cndmask_b32_e64 v25, 0, v25, s[62:63]
	v_cndmask_b32_e64 v26, 0, v26, s[64:65]
	v_cndmask_b32_e64 v27, 0, v27, s[66:67]
	v_mfma_f32_32x32x16_f16 v[56:71], v[184:187], v[204:207], v[56:71]
	v_cvt_pkrtz_f16_f32 v34, v24, v25
	v_cvt_pkrtz_f16_f32 v35, v26, v27
	ds_write2_b64 v3, v[32:33], v[34:35] offset0:0 offset1:66
	s_waitcnt vmcnt(21)
	v_pk_mul_f32 v[24:25], v[16:17], s[34:35] op_sel_hi:[1,0]
	v_pk_mul_f32 v[26:27], v[18:19], s[34:35] op_sel_hi:[1,0]
	v_pk_mul_f32 v[28:29], v[20:21], s[42:43] op_sel_hi:[1,0]
	v_pk_mul_f32 v[30:31], v[22:23], s[42:43] op_sel_hi:[1,0]
	v_mfma_f32_32x32x16_f16 v[72:87], v[184:187], v[12:15], v[72:87]
	v_cmp_lt_i32_e64 s[60:61], 0, v96
	v_cmp_lt_i32_e64 s[62:63], 0, v97
	v_cmp_lt_i32_e64 s[64:65], 0, v98
	v_cmp_lt_i32_e64 s[66:67], 0, v99
	v_max_f32_e32 v24, v24, v28
	v_max_f32_e32 v25, v25, v29
	v_max_f32_e32 v26, v26, v30
	v_max_f32_e32 v27, v27, v31
	v_cndmask_b32_e64 v24, 0, v24, s[60:61]
	v_cndmask_b32_e64 v25, 0, v25, s[62:63]
	v_cndmask_b32_e64 v26, 0, v26, s[64:65]
	v_cndmask_b32_e64 v27, 0, v27, s[66:67]
	v_mfma_f32_32x32x16_f16 v[40:55], v[188:191], v[208:211], v[40:55]
	v_cvt_pkrtz_f16_f32 v32, v24, v25
	v_cvt_pkrtz_f16_f32 v33, v26, v27
	s_waitcnt vmcnt(20)
	v_pk_mul_f32 v[24:25], v[16:17], s[34:35] op_sel:[0,1] op_sel_hi:[1,1]
	v_pk_mul_f32 v[26:27], v[18:19], s[34:35] op_sel:[0,1] op_sel_hi:[1,1]
	v_pk_mul_f32 v[28:29], v[20:21], s[42:43] op_sel:[0,1] op_sel_hi:[1,1]
	v_pk_mul_f32 v[30:31], v[22:23], s[42:43] op_sel:[0,1] op_sel_hi:[1,1]
	v_mfma_f32_32x32x16_f16 v[56:71], v[188:191], v[212:215], v[56:71]
	v_cmp_lt_i32_e64 s[60:61], 0, v100
	v_cmp_lt_i32_e64 s[62:63], 0, v101
	v_cmp_lt_i32_e64 s[64:65], 0, v102
	v_cmp_lt_i32_e64 s[66:67], 0, v103
	v_max_f32_e32 v24, v24, v28
	v_max_f32_e32 v25, v25, v29
	v_max_f32_e32 v26, v26, v30
	v_max_f32_e32 v27, v27, v31
	v_cndmask_b32_e64 v24, 0, v24, s[60:61]
	v_cndmask_b32_e64 v25, 0, v25, s[62:63]
	v_cndmask_b32_e64 v26, 0, v26, s[64:65]
	v_cndmask_b32_e64 v27, 0, v27, s[66:67]
	v_mfma_f32_32x32x16_f16 v[72:87], v[188:191], v[12:15], v[72:87]
	v_cvt_pkrtz_f16_f32 v34, v24, v25
	v_cvt_pkrtz_f16_f32 v35, v26, v27
	ds_write2_b64 v3, v[32:33], v[34:35] offset0:132 offset1:198
	s_waitcnt vmcnt(19)
	v_pk_mul_f32 v[24:25], v[16:17], s[36:37] op_sel_hi:[1,0]
	v_pk_mul_f32 v[26:27], v[18:19], s[36:37] op_sel_hi:[1,0]
	v_pk_mul_f32 v[28:29], v[20:21], s[44:45] op_sel_hi:[1,0]
	v_pk_mul_f32 v[30:31], v[22:23], s[44:45] op_sel_hi:[1,0]
	v_mfma_f32_32x32x16_f16 v[40:55], v[192:195], v[216:219], v[40:55]
	v_cmp_lt_i32_e64 s[60:61], 0, v104
	v_cmp_lt_i32_e64 s[62:63], 0, v105
	v_cmp_lt_i32_e64 s[64:65], 0, v106
	v_cmp_lt_i32_e64 s[66:67], 0, v107
	v_max_f32_e32 v24, v24, v28
	v_max_f32_e32 v25, v25, v29
	v_max_f32_e32 v26, v26, v30
	v_max_f32_e32 v27, v27, v31
	v_cndmask_b32_e64 v24, 0, v24, s[60:61]
	v_cndmask_b32_e64 v25, 0, v25, s[62:63]
	v_cndmask_b32_e64 v26, 0, v26, s[64:65]
	v_cndmask_b32_e64 v27, 0, v27, s[66:67]
	v_mfma_f32_32x32x16_f16 v[56:71], v[192:195], v[220:223], v[56:71]
	v_cvt_pkrtz_f16_f32 v32, v24, v25
	v_cvt_pkrtz_f16_f32 v33, v26, v27
	s_waitcnt vmcnt(18)
	v_pk_mul_f32 v[24:25], v[16:17], s[36:37] op_sel:[0,1] op_sel_hi:[1,1]
	v_pk_mul_f32 v[26:27], v[18:19], s[36:37] op_sel:[0,1] op_sel_hi:[1,1]
	v_pk_mul_f32 v[28:29], v[20:21], s[44:45] op_sel:[0,1] op_sel_hi:[1,1]
	v_pk_mul_f32 v[30:31], v[22:23], s[44:45] op_sel:[0,1] op_sel_hi:[1,1]
	v_mfma_f32_32x32x16_f16 v[72:87], v[192:195], v[12:15], v[72:87]
	v_cmp_lt_i32_e64 s[60:61], 0, v108
	v_cmp_lt_i32_e64 s[62:63], 0, v109
	v_cmp_lt_i32_e64 s[64:65], 0, v110
	v_cmp_lt_i32_e64 s[66:67], 0, v111
	v_max_f32_e32 v24, v24, v28
	v_max_f32_e32 v25, v25, v29
	v_max_f32_e32 v26, v26, v30
	v_max_f32_e32 v27, v27, v31
	v_cndmask_b32_e64 v24, 0, v24, s[60:61]
	v_cndmask_b32_e64 v25, 0, v25, s[62:63]
	v_cndmask_b32_e64 v26, 0, v26, s[64:65]
	v_cndmask_b32_e64 v27, 0, v27, s[66:67]
	v_mfma_f32_32x32x16_f16 v[40:55], v[196:199], v[224:227], v[40:55]
	v_cvt_pkrtz_f16_f32 v34, v24, v25
	v_cvt_pkrtz_f16_f32 v35, v26, v27
	ds_write2_b64 v4, v[32:33], v[34:35] offset0:0 offset1:66
	s_waitcnt vmcnt(17)
	v_pk_mul_f32 v[24:25], v[16:17], s[38:39] op_sel_hi:[1,0]
	v_pk_mul_f32 v[26:27], v[18:19], s[38:39] op_sel_hi:[1,0]
	v_pk_mul_f32 v[28:29], v[20:21], s[46:47] op_sel_hi:[1,0]
	v_pk_mul_f32 v[30:31], v[22:23], s[46:47] op_sel_hi:[1,0]
	v_mfma_f32_32x32x16_f16 v[56:71], v[196:199], v[228:231], v[56:71]
	v_cmp_lt_i32_e64 s[60:61], 0, v112
	v_cmp_lt_i32_e64 s[62:63], 0, v113
	v_cmp_lt_i32_e64 s[64:65], 0, v114
	v_cmp_lt_i32_e64 s[66:67], 0, v115
	v_max_f32_e32 v24, v24, v28
	v_max_f32_e32 v25, v25, v29
	v_max_f32_e32 v26, v26, v30
	v_max_f32_e32 v27, v27, v31
	v_cndmask_b32_e64 v24, 0, v24, s[60:61]
	v_cndmask_b32_e64 v25, 0, v25, s[62:63]
	v_cndmask_b32_e64 v26, 0, v26, s[64:65]
	v_cndmask_b32_e64 v27, 0, v27, s[66:67]
	v_cvt_pkrtz_f16_f32 v32, v24, v25
	v_cvt_pkrtz_f16_f32 v33, v26, v27
	s_waitcnt vmcnt(16)
	v_pk_mul_f32 v[24:25], v[16:17], s[38:39] op_sel:[0,1] op_sel_hi:[1,1]
	v_pk_mul_f32 v[26:27], v[18:19], s[38:39] op_sel:[0,1] op_sel_hi:[1,1]
	v_pk_mul_f32 v[28:29], v[20:21], s[46:47] op_sel:[0,1] op_sel_hi:[1,1]
	v_pk_mul_f32 v[30:31], v[22:23], s[46:47] op_sel:[0,1] op_sel_hi:[1,1]
	v_mfma_f32_32x32x16_f16 v[72:87], v[196:199], v[12:15], v[72:87]
	v_cmp_lt_i32_e64 s[60:61], 0, v116
	v_cmp_lt_i32_e64 s[62:63], 0, v117
	v_cmp_lt_i32_e64 s[64:65], 0, v118
	v_cmp_lt_i32_e64 s[66:67], 0, v119
	v_max_f32_e32 v24, v24, v28
	v_max_f32_e32 v25, v25, v29
	v_max_f32_e32 v26, v26, v30
	v_max_f32_e32 v27, v27, v31
	v_cndmask_b32_e64 v24, 0, v24, s[60:61]
	v_cndmask_b32_e64 v25, 0, v25, s[62:63]
	v_cndmask_b32_e64 v26, 0, v26, s[64:65]
	v_cndmask_b32_e64 v27, 0, v27, s[66:67]
	v_cvt_pkrtz_f16_f32 v34, v24, v25
	v_cvt_pkrtz_f16_f32 v35, v26, v27
	ds_write2_b64 v4, v[32:33], v[34:35] offset0:132 offset1:198
	s_waitcnt vmcnt(12)
	ds_write_b128 v9, v[152:155] offset:0
	ds_write_b128 v9, v[156:159] offset:1024
	ds_write_b128 v9, v[160:163] offset:2048
	ds_write_b128 v9, v[164:167] offset:3072
	s_add_u32 s3, s19, 3
	s_and_b32 s3, s3, 7
	s_lshl_b32 s3, s3, 10
	v_add_u32_e32 v11, s3, v10
	ds_read_b128 v[16:19], v11
	ds_read_b128 v[20:23], v11 offset:8192
	s_waitcnt lgkmcnt(0)
	s_barrier
	ds_read_b128 v[184:187], v7 offset:0
	ds_read_b128 v[200:203], v8 offset:0
	ds_read_b128 v[204:207], v8 offset:1024
	ds_read_b128 v[188:191], v7 offset:32
	ds_read_b128 v[208:211], v8 offset:2048
	ds_read_b128 v[212:215], v8 offset:3072
	ds_read_b128 v[192:195], v7 offset:64
	ds_read_b128 v[216:219], v8 offset:4096
	ds_read_b128 v[220:223], v8 offset:5120
	ds_read_b128 v[196:199], v7 offset:96
	ds_read_b128 v[224:227], v8 offset:6144
	ds_read_b128 v[228:231], v8 offset:7168
	s_add_u32 s3, s19, 4
	s_and_b32 s3, s3, 7
	s_lshl_b32 s57, s3, 10
	s_add_u32 s48, s57, s22
	s_add_u32 s49, s48, 0x2000
	s_add_u32 s50, s48, 0x4000
	s_add_u32 s51, s48, 0x6000
	s_add_u32 s52, s48, 0x8000
	s_add_u32 s53, s48, 0xa000
	s_add_u32 s54, s48, 0xc000
	s_add_u32 s55, s48, 0xe000
	s_lshl_b32 s56, s3, 15
	s_add_u32 s56, s56, s23
	buffer_load_dwordx4 v[88:91], v1, s[4:7], s48 offen nt
	buffer_load_dwordx4 v[92:95], v1, s[4:7], s49 offen nt
	buffer_load_dwordx4 v[96:99], v1, s[4:7], s50 offen nt
	buffer_load_dwordx4 v[100:103], v1, s[4:7], s51 offen nt
	buffer_load_dwordx4 v[104:107], v1, s[4:7], s52 offen nt
	buffer_load_dwordx4 v[108:111], v1, s[4:7], s53 offen nt
	buffer_load_dwordx4 v[112:115], v1, s[4:7], s54 offen nt
	buffer_load_dwordx4 v[116:119], v1, s[4:7], s55 offen nt
	buffer_load_dwordx4 v[152:155], v1, s[8:11], s56 offen
	buffer_load_dwordx4 v[156:159], v1, s[8:11], s56 offen offset:1024
	buffer_load_dwordx4 v[160:163], v1, s[8:11], s56 offen offset:2048
	buffer_load_dwordx4 v[164:167], v1, s[8:11], s56 offen offset:3072
	s_waitcnt vmcnt(23)
	v_pk_mul_f32 v[24:25], v[16:17], s[32:33] op_sel_hi:[1,0]
	v_pk_mul_f32 v[26:27], v[18:19], s[32:33] op_sel_hi:[1,0]
	v_pk_mul_f32 v[28:29], v[20:21], s[40:41] op_sel_hi:[1,0]
	v_pk_mul_f32 v[30:31], v[22:23], s[40:41] op_sel_hi:[1,0]
	v_cmp_lt_i32_e64 s[60:61], 0, v120
	v_cmp_lt_i32_e64 s[62:63], 0, v121
	v_cmp_lt_i32_e64 s[64:65], 0, v122
	v_cmp_lt_i32_e64 s[66:67], 0, v123
	v_max_f32_e32 v24, v24, v28
	v_max_f32_e32 v25, v25, v29
	v_max_f32_e32 v26, v26, v30
	v_max_f32_e32 v27, v27, v31
	v_cndmask_b32_e64 v24, 0, v24, s[60:61]
	v_cndmask_b32_e64 v25, 0, v25, s[62:63]
	v_cndmask_b32_e64 v26, 0, v26, s[64:65]
	v_cndmask_b32_e64 v27, 0, v27, s[66:67]
	v_cvt_pkrtz_f16_f32 v32, v24, v25
	v_cvt_pkrtz_f16_f32 v33, v26, v27
	s_waitcnt vmcnt(22)
	s_waitcnt lgkmcnt(0)
	v_pk_mul_f32 v[24:25], v[16:17], s[32:33] op_sel:[0,1] op_sel_hi:[1,1]
	v_pk_mul_f32 v[26:27], v[18:19], s[32:33] op_sel:[0,1] op_sel_hi:[1,1]
	v_pk_mul_f32 v[28:29], v[20:21], s[40:41] op_sel:[0,1] op_sel_hi:[1,1]
	v_pk_mul_f32 v[30:31], v[22:23], s[40:41] op_sel:[0,1] op_sel_hi:[1,1]
	v_mfma_f32_32x32x16_f16 v[40:55], v[184:187], v[200:203], v[40:55]
	v_cmp_lt_i32_e64 s[60:61], 0, v124
	v_cmp_lt_i32_e64 s[62:63], 0, v125
	v_cmp_lt_i32_e64 s[64:65], 0, v126
	v_cmp_lt_i32_e64 s[66:67], 0, v127
	v_max_f32_e32 v24, v24, v28
	v_max_f32_e32 v25, v25, v29
	v_max_f32_e32 v26, v26, v30
	v_max_f32_e32 v27, v27, v31
	v_cndmask_b32_e64 v24, 0, v24, s[60:61]
	v_cndmask_b32_e64 v25, 0, v25, s[62:63]
	v_cndmask_b32_e64 v26, 0, v26, s[64:65]
	v_cndmask_b32_e64 v27, 0, v27, s[66:67]
	v_mfma_f32_32x32x16_f16 v[56:71], v[184:187], v[204:207], v[56:71]
	v_cvt_pkrtz_f16_f32 v34, v24, v25
	v_cvt_pkrtz_f16_f32 v35, v26, v27
	ds_write2_b64 v5, v[32:33], v[34:35] offset0:0 offset1:66
	s_waitcnt vmcnt(21)
	v_pk_mul_f32 v[24:25], v[16:17], s[34:35] op_sel_hi:[1,0]
	v_pk_mul_f32 v[26:27], v[18:19], s[34:35] op_sel_hi:[1,0]
	v_pk_mul_f32 v[28:29], v[20:21], s[42:43] op_sel_hi:[1,0]
	v_pk_mul_f32 v[30:31], v[22:23], s[42:43] op_sel_hi:[1,0]
	v_mfma_f32_32x32x16_f16 v[72:87], v[184:187], v[12:15], v[72:87]
	v_cmp_lt_i32_e64 s[60:61], 0, v128
	v_cmp_lt_i32_e64 s[62:63], 0, v129
	v_cmp_lt_i32_e64 s[64:65], 0, v130
	v_cmp_lt_i32_e64 s[66:67], 0, v131
	v_max_f32_e32 v24, v24, v28
	v_max_f32_e32 v25, v25, v29
	v_max_f32_e32 v26, v26, v30
	v_max_f32_e32 v27, v27, v31
	v_cndmask_b32_e64 v24, 0, v24, s[60:61]
	v_cndmask_b32_e64 v25, 0, v25, s[62:63]
	v_cndmask_b32_e64 v26, 0, v26, s[64:65]
	v_cndmask_b32_e64 v27, 0, v27, s[66:67]
	v_mfma_f32_32x32x16_f16 v[40:55], v[188:191], v[208:211], v[40:55]
	v_cvt_pkrtz_f16_f32 v32, v24, v25
	v_cvt_pkrtz_f16_f32 v33, v26, v27
	s_waitcnt vmcnt(20)
	v_pk_mul_f32 v[24:25], v[16:17], s[34:35] op_sel:[0,1] op_sel_hi:[1,1]
	v_pk_mul_f32 v[26:27], v[18:19], s[34:35] op_sel:[0,1] op_sel_hi:[1,1]
	v_pk_mul_f32 v[28:29], v[20:21], s[42:43] op_sel:[0,1] op_sel_hi:[1,1]
	v_pk_mul_f32 v[30:31], v[22:23], s[42:43] op_sel:[0,1] op_sel_hi:[1,1]
	v_mfma_f32_32x32x16_f16 v[56:71], v[188:191], v[212:215], v[56:71]
	v_cmp_lt_i32_e64 s[60:61], 0, v132
	v_cmp_lt_i32_e64 s[62:63], 0, v133
	v_cmp_lt_i32_e64 s[64:65], 0, v134
	v_cmp_lt_i32_e64 s[66:67], 0, v135
	v_max_f32_e32 v24, v24, v28
	v_max_f32_e32 v25, v25, v29
	v_max_f32_e32 v26, v26, v30
	v_max_f32_e32 v27, v27, v31
	v_cndmask_b32_e64 v24, 0, v24, s[60:61]
	v_cndmask_b32_e64 v25, 0, v25, s[62:63]
	v_cndmask_b32_e64 v26, 0, v26, s[64:65]
	v_cndmask_b32_e64 v27, 0, v27, s[66:67]
	v_mfma_f32_32x32x16_f16 v[72:87], v[188:191], v[12:15], v[72:87]
	v_cvt_pkrtz_f16_f32 v34, v24, v25
	v_cvt_pkrtz_f16_f32 v35, v26, v27
	ds_write2_b64 v5, v[32:33], v[34:35] offset0:132 offset1:198
	s_waitcnt vmcnt(19)
	v_pk_mul_f32 v[24:25], v[16:17], s[36:37] op_sel_hi:[1,0]
	v_pk_mul_f32 v[26:27], v[18:19], s[36:37] op_sel_hi:[1,0]
	v_pk_mul_f32 v[28:29], v[20:21], s[44:45] op_sel_hi:[1,0]
	v_pk_mul_f32 v[30:31], v[22:23], s[44:45] op_sel_hi:[1,0]
	v_mfma_f32_32x32x16_f16 v[40:55], v[192:195], v[216:219], v[40:55]
	v_cmp_lt_i32_e64 s[60:61], 0, v136
	v_cmp_lt_i32_e64 s[62:63], 0, v137
	v_cmp_lt_i32_e64 s[64:65], 0, v138
	v_cmp_lt_i32_e64 s[66:67], 0, v139
	v_max_f32_e32 v24, v24, v28
	v_max_f32_e32 v25, v25, v29
	v_max_f32_e32 v26, v26, v30
	v_max_f32_e32 v27, v27, v31
	v_cndmask_b32_e64 v24, 0, v24, s[60:61]
	v_cndmask_b32_e64 v25, 0, v25, s[62:63]
	v_cndmask_b32_e64 v26, 0, v26, s[64:65]
	v_cndmask_b32_e64 v27, 0, v27, s[66:67]
	v_mfma_f32_32x32x16_f16 v[56:71], v[192:195], v[220:223], v[56:71]
	v_cvt_pkrtz_f16_f32 v32, v24, v25
	v_cvt_pkrtz_f16_f32 v33, v26, v27
	s_waitcnt vmcnt(18)
	v_pk_mul_f32 v[24:25], v[16:17], s[36:37] op_sel:[0,1] op_sel_hi:[1,1]
	v_pk_mul_f32 v[26:27], v[18:19], s[36:37] op_sel:[0,1] op_sel_hi:[1,1]
	v_pk_mul_f32 v[28:29], v[20:21], s[44:45] op_sel:[0,1] op_sel_hi:[1,1]
	v_pk_mul_f32 v[30:31], v[22:23], s[44:45] op_sel:[0,1] op_sel_hi:[1,1]
	v_mfma_f32_32x32x16_f16 v[72:87], v[192:195], v[12:15], v[72:87]
	v_cmp_lt_i32_e64 s[60:61], 0, v140
	v_cmp_lt_i32_e64 s[62:63], 0, v141
	v_cmp_lt_i32_e64 s[64:65], 0, v142
	v_cmp_lt_i32_e64 s[66:67], 0, v143
	v_max_f32_e32 v24, v24, v28
	v_max_f32_e32 v25, v25, v29
	v_max_f32_e32 v26, v26, v30
	v_max_f32_e32 v27, v27, v31
	v_cndmask_b32_e64 v24, 0, v24, s[60:61]
	v_cndmask_b32_e64 v25, 0, v25, s[62:63]
	v_cndmask_b32_e64 v26, 0, v26, s[64:65]
	v_cndmask_b32_e64 v27, 0, v27, s[66:67]
	v_mfma_f32_32x32x16_f16 v[40:55], v[196:199], v[224:227], v[40:55]
	v_cvt_pkrtz_f16_f32 v34, v24, v25
	v_cvt_pkrtz_f16_f32 v35, v26, v27
	ds_write2_b64 v6, v[32:33], v[34:35] offset0:0 offset1:66
	s_waitcnt vmcnt(17)
	v_pk_mul_f32 v[24:25], v[16:17], s[38:39] op_sel_hi:[1,0]
	v_pk_mul_f32 v[26:27], v[18:19], s[38:39] op_sel_hi:[1,0]
	v_pk_mul_f32 v[28:29], v[20:21], s[46:47] op_sel_hi:[1,0]
	v_pk_mul_f32 v[30:31], v[22:23], s[46:47] op_sel_hi:[1,0]
	v_mfma_f32_32x32x16_f16 v[56:71], v[196:199], v[228:231], v[56:71]
	v_cmp_lt_i32_e64 s[60:61], 0, v144
	v_cmp_lt_i32_e64 s[62:63], 0, v145
	v_cmp_lt_i32_e64 s[64:65], 0, v146
	v_cmp_lt_i32_e64 s[66:67], 0, v147
	v_max_f32_e32 v24, v24, v28
	v_max_f32_e32 v25, v25, v29
	v_max_f32_e32 v26, v26, v30
	v_max_f32_e32 v27, v27, v31
	v_cndmask_b32_e64 v24, 0, v24, s[60:61]
	v_cndmask_b32_e64 v25, 0, v25, s[62:63]
	v_cndmask_b32_e64 v26, 0, v26, s[64:65]
	v_cndmask_b32_e64 v27, 0, v27, s[66:67]
	v_cvt_pkrtz_f16_f32 v32, v24, v25
	v_cvt_pkrtz_f16_f32 v33, v26, v27
	s_waitcnt vmcnt(16)
	v_pk_mul_f32 v[24:25], v[16:17], s[38:39] op_sel:[0,1] op_sel_hi:[1,1]
	v_pk_mul_f32 v[26:27], v[18:19], s[38:39] op_sel:[0,1] op_sel_hi:[1,1]
	v_pk_mul_f32 v[28:29], v[20:21], s[46:47] op_sel:[0,1] op_sel_hi:[1,1]
	v_pk_mul_f32 v[30:31], v[22:23], s[46:47] op_sel:[0,1] op_sel_hi:[1,1]
	v_mfma_f32_32x32x16_f16 v[72:87], v[196:199], v[12:15], v[72:87]
	v_cmp_lt_i32_e64 s[60:61], 0, v148
	v_cmp_lt_i32_e64 s[62:63], 0, v149
	v_cmp_lt_i32_e64 s[64:65], 0, v150
	v_cmp_lt_i32_e64 s[66:67], 0, v151
	v_max_f32_e32 v24, v24, v28
	v_max_f32_e32 v25, v25, v29
	v_max_f32_e32 v26, v26, v30
	v_max_f32_e32 v27, v27, v31
	v_cndmask_b32_e64 v24, 0, v24, s[60:61]
	v_cndmask_b32_e64 v25, 0, v25, s[62:63]
	v_cndmask_b32_e64 v26, 0, v26, s[64:65]
	v_cndmask_b32_e64 v27, 0, v27, s[66:67]
	v_cvt_pkrtz_f16_f32 v34, v24, v25
	v_cvt_pkrtz_f16_f32 v35, v26, v27
	ds_write2_b64 v6, v[32:33], v[34:35] offset0:132 offset1:198
	s_waitcnt vmcnt(12)
	ds_write_b128 v9, v[168:171] offset:32768
	ds_write_b128 v9, v[172:175] offset:33792
	ds_write_b128 v9, v[176:179] offset:34816
	ds_write_b128 v9, v[180:183] offset:35840
	s_add_u32 s3, s19, 4
	s_and_b32 s3, s3, 7
	s_lshl_b32 s3, s3, 10
	v_add_u32_e32 v11, s3, v10
	ds_read_b128 v[16:19], v11
	ds_read_b128 v[20:23], v11 offset:8192
	s_waitcnt lgkmcnt(0)
	s_barrier
	ds_read_b128 v[184:187], v7 offset:33792
	ds_read_b128 v[200:203], v8 offset:32768
	ds_read_b128 v[204:207], v8 offset:33792
	ds_read_b128 v[188:191], v7 offset:33824
	ds_read_b128 v[208:211], v8 offset:34816
	ds_read_b128 v[212:215], v8 offset:35840
	ds_read_b128 v[192:195], v7 offset:33856
	ds_read_b128 v[216:219], v8 offset:36864
	ds_read_b128 v[220:223], v8 offset:37888
	ds_read_b128 v[196:199], v7 offset:33888
	ds_read_b128 v[224:227], v8 offset:38912
	ds_read_b128 v[228:231], v8 offset:39936
	s_add_u32 s3, s19, 5
	s_and_b32 s3, s3, 7
	s_lshl_b32 s57, s3, 10
	s_add_u32 s48, s57, s22
	s_add_u32 s49, s48, 0x2000
	s_add_u32 s50, s48, 0x4000
	s_add_u32 s51, s48, 0x6000
	s_add_u32 s52, s48, 0x8000
	s_add_u32 s53, s48, 0xa000
	s_add_u32 s54, s48, 0xc000
	s_add_u32 s55, s48, 0xe000
	s_lshl_b32 s56, s3, 15
	s_add_u32 s56, s56, s23
	buffer_load_dwordx4 v[120:123], v1, s[4:7], s48 offen nt
	buffer_load_dwordx4 v[124:127], v1, s[4:7], s49 offen nt
	buffer_load_dwordx4 v[128:131], v1, s[4:7], s50 offen nt
	buffer_load_dwordx4 v[132:135], v1, s[4:7], s51 offen nt
	buffer_load_dwordx4 v[136:139], v1, s[4:7], s52 offen nt
	buffer_load_dwordx4 v[140:143], v1, s[4:7], s53 offen nt
	buffer_load_dwordx4 v[144:147], v1, s[4:7], s54 offen nt
	buffer_load_dwordx4 v[148:151], v1, s[4:7], s55 offen nt
	buffer_load_dwordx4 v[168:171], v1, s[8:11], s56 offen
	buffer_load_dwordx4 v[172:175], v1, s[8:11], s56 offen offset:1024
	buffer_load_dwordx4 v[176:179], v1, s[8:11], s56 offen offset:2048
	buffer_load_dwordx4 v[180:183], v1, s[8:11], s56 offen offset:3072
	s_waitcnt vmcnt(23)
	v_pk_mul_f32 v[24:25], v[16:17], s[32:33] op_sel_hi:[1,0]
	v_pk_mul_f32 v[26:27], v[18:19], s[32:33] op_sel_hi:[1,0]
	v_pk_mul_f32 v[28:29], v[20:21], s[40:41] op_sel_hi:[1,0]
	v_pk_mul_f32 v[30:31], v[22:23], s[40:41] op_sel_hi:[1,0]
	v_cmp_lt_i32_e64 s[60:61], 0, v88
	v_cmp_lt_i32_e64 s[62:63], 0, v89
	v_cmp_lt_i32_e64 s[64:65], 0, v90
	v_cmp_lt_i32_e64 s[66:67], 0, v91
	v_max_f32_e32 v24, v24, v28
	v_max_f32_e32 v25, v25, v29
	v_max_f32_e32 v26, v26, v30
	v_max_f32_e32 v27, v27, v31
	v_cndmask_b32_e64 v24, 0, v24, s[60:61]
	v_cndmask_b32_e64 v25, 0, v25, s[62:63]
	v_cndmask_b32_e64 v26, 0, v26, s[64:65]
	v_cndmask_b32_e64 v27, 0, v27, s[66:67]
	v_cvt_pkrtz_f16_f32 v32, v24, v25
	v_cvt_pkrtz_f16_f32 v33, v26, v27
	s_waitcnt vmcnt(22)
	s_waitcnt lgkmcnt(0)
	v_pk_mul_f32 v[24:25], v[16:17], s[32:33] op_sel:[0,1] op_sel_hi:[1,1]
	v_pk_mul_f32 v[26:27], v[18:19], s[32:33] op_sel:[0,1] op_sel_hi:[1,1]
	v_pk_mul_f32 v[28:29], v[20:21], s[40:41] op_sel:[0,1] op_sel_hi:[1,1]
	v_pk_mul_f32 v[30:31], v[22:23], s[40:41] op_sel:[0,1] op_sel_hi:[1,1]
	v_mfma_f32_32x32x16_f16 v[40:55], v[184:187], v[200:203], v[40:55]
	v_cmp_lt_i32_e64 s[60:61], 0, v92
	v_cmp_lt_i32_e64 s[62:63], 0, v93
	v_cmp_lt_i32_e64 s[64:65], 0, v94
	v_cmp_lt_i32_e64 s[66:67], 0, v95
	v_max_f32_e32 v24, v24, v28
	v_max_f32_e32 v25, v25, v29
	v_max_f32_e32 v26, v26, v30
	v_max_f32_e32 v27, v27, v31
	v_cndmask_b32_e64 v24, 0, v24, s[60:61]
	v_cndmask_b32_e64 v25, 0, v25, s[62:63]
	v_cndmask_b32_e64 v26, 0, v26, s[64:65]
	v_cndmask_b32_e64 v27, 0, v27, s[66:67]
	v_mfma_f32_32x32x16_f16 v[56:71], v[184:187], v[204:207], v[56:71]
	v_cvt_pkrtz_f16_f32 v34, v24, v25
	v_cvt_pkrtz_f16_f32 v35, v26, v27
	ds_write2_b64 v3, v[32:33], v[34:35] offset0:0 offset1:66
	s_waitcnt vmcnt(21)
	v_pk_mul_f32 v[24:25], v[16:17], s[34:35] op_sel_hi:[1,0]
	v_pk_mul_f32 v[26:27], v[18:19], s[34:35] op_sel_hi:[1,0]
	v_pk_mul_f32 v[28:29], v[20:21], s[42:43] op_sel_hi:[1,0]
	v_pk_mul_f32 v[30:31], v[22:23], s[42:43] op_sel_hi:[1,0]
	v_mfma_f32_32x32x16_f16 v[72:87], v[184:187], v[12:15], v[72:87]
	v_cmp_lt_i32_e64 s[60:61], 0, v96
	v_cmp_lt_i32_e64 s[62:63], 0, v97
	v_cmp_lt_i32_e64 s[64:65], 0, v98
	v_cmp_lt_i32_e64 s[66:67], 0, v99
	v_max_f32_e32 v24, v24, v28
	v_max_f32_e32 v25, v25, v29
	v_max_f32_e32 v26, v26, v30
	v_max_f32_e32 v27, v27, v31
	v_cndmask_b32_e64 v24, 0, v24, s[60:61]
	v_cndmask_b32_e64 v25, 0, v25, s[62:63]
	v_cndmask_b32_e64 v26, 0, v26, s[64:65]
	v_cndmask_b32_e64 v27, 0, v27, s[66:67]
	v_mfma_f32_32x32x16_f16 v[40:55], v[188:191], v[208:211], v[40:55]
	v_cvt_pkrtz_f16_f32 v32, v24, v25
	v_cvt_pkrtz_f16_f32 v33, v26, v27
	s_waitcnt vmcnt(20)
	v_pk_mul_f32 v[24:25], v[16:17], s[34:35] op_sel:[0,1] op_sel_hi:[1,1]
	v_pk_mul_f32 v[26:27], v[18:19], s[34:35] op_sel:[0,1] op_sel_hi:[1,1]
	v_pk_mul_f32 v[28:29], v[20:21], s[42:43] op_sel:[0,1] op_sel_hi:[1,1]
	v_pk_mul_f32 v[30:31], v[22:23], s[42:43] op_sel:[0,1] op_sel_hi:[1,1]
	v_mfma_f32_32x32x16_f16 v[56:71], v[188:191], v[212:215], v[56:71]
	v_cmp_lt_i32_e64 s[60:61], 0, v100
	v_cmp_lt_i32_e64 s[62:63], 0, v101
	v_cmp_lt_i32_e64 s[64:65], 0, v102
	v_cmp_lt_i32_e64 s[66:67], 0, v103
	v_max_f32_e32 v24, v24, v28
	v_max_f32_e32 v25, v25, v29
	v_max_f32_e32 v26, v26, v30
	v_max_f32_e32 v27, v27, v31
	v_cndmask_b32_e64 v24, 0, v24, s[60:61]
	v_cndmask_b32_e64 v25, 0, v25, s[62:63]
	v_cndmask_b32_e64 v26, 0, v26, s[64:65]
	v_cndmask_b32_e64 v27, 0, v27, s[66:67]
	v_mfma_f32_32x32x16_f16 v[72:87], v[188:191], v[12:15], v[72:87]
	v_cvt_pkrtz_f16_f32 v34, v24, v25
	v_cvt_pkrtz_f16_f32 v35, v26, v27
	ds_write2_b64 v3, v[32:33], v[34:35] offset0:132 offset1:198
	s_waitcnt vmcnt(19)
	v_pk_mul_f32 v[24:25], v[16:17], s[36:37] op_sel_hi:[1,0]
	v_pk_mul_f32 v[26:27], v[18:19], s[36:37] op_sel_hi:[1,0]
	v_pk_mul_f32 v[28:29], v[20:21], s[44:45] op_sel_hi:[1,0]
	v_pk_mul_f32 v[30:31], v[22:23], s[44:45] op_sel_hi:[1,0]
	v_mfma_f32_32x32x16_f16 v[40:55], v[192:195], v[216:219], v[40:55]
	v_cmp_lt_i32_e64 s[60:61], 0, v104
	v_cmp_lt_i32_e64 s[62:63], 0, v105
	v_cmp_lt_i32_e64 s[64:65], 0, v106
	v_cmp_lt_i32_e64 s[66:67], 0, v107
	v_max_f32_e32 v24, v24, v28
	v_max_f32_e32 v25, v25, v29
	v_max_f32_e32 v26, v26, v30
	v_max_f32_e32 v27, v27, v31
	v_cndmask_b32_e64 v24, 0, v24, s[60:61]
	v_cndmask_b32_e64 v25, 0, v25, s[62:63]
	v_cndmask_b32_e64 v26, 0, v26, s[64:65]
	v_cndmask_b32_e64 v27, 0, v27, s[66:67]
	v_mfma_f32_32x32x16_f16 v[56:71], v[192:195], v[220:223], v[56:71]
	v_cvt_pkrtz_f16_f32 v32, v24, v25
	v_cvt_pkrtz_f16_f32 v33, v26, v27
	s_waitcnt vmcnt(18)
	v_pk_mul_f32 v[24:25], v[16:17], s[36:37] op_sel:[0,1] op_sel_hi:[1,1]
	v_pk_mul_f32 v[26:27], v[18:19], s[36:37] op_sel:[0,1] op_sel_hi:[1,1]
	v_pk_mul_f32 v[28:29], v[20:21], s[44:45] op_sel:[0,1] op_sel_hi:[1,1]
	v_pk_mul_f32 v[30:31], v[22:23], s[44:45] op_sel:[0,1] op_sel_hi:[1,1]
	v_mfma_f32_32x32x16_f16 v[72:87], v[192:195], v[12:15], v[72:87]
	v_cmp_lt_i32_e64 s[60:61], 0, v108
	v_cmp_lt_i32_e64 s[62:63], 0, v109
	v_cmp_lt_i32_e64 s[64:65], 0, v110
	v_cmp_lt_i32_e64 s[66:67], 0, v111
	v_max_f32_e32 v24, v24, v28
	v_max_f32_e32 v25, v25, v29
	v_max_f32_e32 v26, v26, v30
	v_max_f32_e32 v27, v27, v31
	v_cndmask_b32_e64 v24, 0, v24, s[60:61]
	v_cndmask_b32_e64 v25, 0, v25, s[62:63]
	v_cndmask_b32_e64 v26, 0, v26, s[64:65]
	v_cndmask_b32_e64 v27, 0, v27, s[66:67]
	v_mfma_f32_32x32x16_f16 v[40:55], v[196:199], v[224:227], v[40:55]
	v_cvt_pkrtz_f16_f32 v34, v24, v25
	v_cvt_pkrtz_f16_f32 v35, v26, v27
	ds_write2_b64 v4, v[32:33], v[34:35] offset0:0 offset1:66
	s_waitcnt vmcnt(17)
	v_pk_mul_f32 v[24:25], v[16:17], s[38:39] op_sel_hi:[1,0]
	v_pk_mul_f32 v[26:27], v[18:19], s[38:39] op_sel_hi:[1,0]
	v_pk_mul_f32 v[28:29], v[20:21], s[46:47] op_sel_hi:[1,0]
	v_pk_mul_f32 v[30:31], v[22:23], s[46:47] op_sel_hi:[1,0]
	v_mfma_f32_32x32x16_f16 v[56:71], v[196:199], v[228:231], v[56:71]
	v_cmp_lt_i32_e64 s[60:61], 0, v112
	v_cmp_lt_i32_e64 s[62:63], 0, v113
	v_cmp_lt_i32_e64 s[64:65], 0, v114
	v_cmp_lt_i32_e64 s[66:67], 0, v115
	v_max_f32_e32 v24, v24, v28
	v_max_f32_e32 v25, v25, v29
	v_max_f32_e32 v26, v26, v30
	v_max_f32_e32 v27, v27, v31
	v_cndmask_b32_e64 v24, 0, v24, s[60:61]
	v_cndmask_b32_e64 v25, 0, v25, s[62:63]
	v_cndmask_b32_e64 v26, 0, v26, s[64:65]
	v_cndmask_b32_e64 v27, 0, v27, s[66:67]
	v_cvt_pkrtz_f16_f32 v32, v24, v25
	v_cvt_pkrtz_f16_f32 v33, v26, v27
	s_waitcnt vmcnt(16)
	v_pk_mul_f32 v[24:25], v[16:17], s[38:39] op_sel:[0,1] op_sel_hi:[1,1]
	v_pk_mul_f32 v[26:27], v[18:19], s[38:39] op_sel:[0,1] op_sel_hi:[1,1]
	v_pk_mul_f32 v[28:29], v[20:21], s[46:47] op_sel:[0,1] op_sel_hi:[1,1]
	v_pk_mul_f32 v[30:31], v[22:23], s[46:47] op_sel:[0,1] op_sel_hi:[1,1]
	v_mfma_f32_32x32x16_f16 v[72:87], v[196:199], v[12:15], v[72:87]
	v_cmp_lt_i32_e64 s[60:61], 0, v116
	v_cmp_lt_i32_e64 s[62:63], 0, v117
	v_cmp_lt_i32_e64 s[64:65], 0, v118
	v_cmp_lt_i32_e64 s[66:67], 0, v119
	v_max_f32_e32 v24, v24, v28
	v_max_f32_e32 v25, v25, v29
	v_max_f32_e32 v26, v26, v30
	v_max_f32_e32 v27, v27, v31
	v_cndmask_b32_e64 v24, 0, v24, s[60:61]
	v_cndmask_b32_e64 v25, 0, v25, s[62:63]
	v_cndmask_b32_e64 v26, 0, v26, s[64:65]
	v_cndmask_b32_e64 v27, 0, v27, s[66:67]
	v_cvt_pkrtz_f16_f32 v34, v24, v25
	v_cvt_pkrtz_f16_f32 v35, v26, v27
	ds_write2_b64 v4, v[32:33], v[34:35] offset0:132 offset1:198
	s_waitcnt vmcnt(12)
	ds_write_b128 v9, v[152:155] offset:0
	ds_write_b128 v9, v[156:159] offset:1024
	ds_write_b128 v9, v[160:163] offset:2048
	ds_write_b128 v9, v[164:167] offset:3072
	s_add_u32 s3, s19, 5
	s_and_b32 s3, s3, 7
	s_lshl_b32 s3, s3, 10
	v_add_u32_e32 v11, s3, v10
	ds_read_b128 v[16:19], v11
	ds_read_b128 v[20:23], v11 offset:8192
	s_waitcnt lgkmcnt(0)
	s_barrier
	ds_read_b128 v[184:187], v7 offset:0
	ds_read_b128 v[200:203], v8 offset:0
	ds_read_b128 v[204:207], v8 offset:1024
	ds_read_b128 v[188:191], v7 offset:32
	ds_read_b128 v[208:211], v8 offset:2048
	ds_read_b128 v[212:215], v8 offset:3072
	ds_read_b128 v[192:195], v7 offset:64
	ds_read_b128 v[216:219], v8 offset:4096
	ds_read_b128 v[220:223], v8 offset:5120
	ds_read_b128 v[196:199], v7 offset:96
	ds_read_b128 v[224:227], v8 offset:6144
	ds_read_b128 v[228:231], v8 offset:7168
	s_add_u32 s3, s19, 6
	s_and_b32 s3, s3, 7
	s_lshl_b32 s57, s3, 10
	s_add_u32 s48, s57, s22
	s_add_u32 s49, s48, 0x2000
	s_add_u32 s50, s48, 0x4000
	s_add_u32 s51, s48, 0x6000
	s_add_u32 s52, s48, 0x8000
	s_add_u32 s53, s48, 0xa000
	s_add_u32 s54, s48, 0xc000
	s_add_u32 s55, s48, 0xe000
	s_lshl_b32 s56, s3, 15
	s_add_u32 s56, s56, s23
	buffer_load_dwordx4 v[88:91], v1, s[4:7], s48 offen nt
	buffer_load_dwordx4 v[92:95], v1, s[4:7], s49 offen nt
	buffer_load_dwordx4 v[96:99], v1, s[4:7], s50 offen nt
	buffer_load_dwordx4 v[100:103], v1, s[4:7], s51 offen nt
	buffer_load_dwordx4 v[104:107], v1, s[4:7], s52 offen nt
	buffer_load_dwordx4 v[108:111], v1, s[4:7], s53 offen nt
	buffer_load_dwordx4 v[112:115], v1, s[4:7], s54 offen nt
	buffer_load_dwordx4 v[116:119], v1, s[4:7], s55 offen nt
	buffer_load_dwordx4 v[152:155], v1, s[8:11], s56 offen
	buffer_load_dwordx4 v[156:159], v1, s[8:11], s56 offen offset:1024
	buffer_load_dwordx4 v[160:163], v1, s[8:11], s56 offen offset:2048
	buffer_load_dwordx4 v[164:167], v1, s[8:11], s56 offen offset:3072
	s_waitcnt vmcnt(23)
	v_pk_mul_f32 v[24:25], v[16:17], s[32:33] op_sel_hi:[1,0]
	v_pk_mul_f32 v[26:27], v[18:19], s[32:33] op_sel_hi:[1,0]
	v_pk_mul_f32 v[28:29], v[20:21], s[40:41] op_sel_hi:[1,0]
	v_pk_mul_f32 v[30:31], v[22:23], s[40:41] op_sel_hi:[1,0]
	v_cmp_lt_i32_e64 s[60:61], 0, v120
	v_cmp_lt_i32_e64 s[62:63], 0, v121
	v_cmp_lt_i32_e64 s[64:65], 0, v122
	v_cmp_lt_i32_e64 s[66:67], 0, v123
	v_max_f32_e32 v24, v24, v28
	v_max_f32_e32 v25, v25, v29
	v_max_f32_e32 v26, v26, v30
	v_max_f32_e32 v27, v27, v31
	v_cndmask_b32_e64 v24, 0, v24, s[60:61]
	v_cndmask_b32_e64 v25, 0, v25, s[62:63]
	v_cndmask_b32_e64 v26, 0, v26, s[64:65]
	v_cndmask_b32_e64 v27, 0, v27, s[66:67]
	v_cvt_pkrtz_f16_f32 v32, v24, v25
	v_cvt_pkrtz_f16_f32 v33, v26, v27
	s_waitcnt vmcnt(22)
	s_waitcnt lgkmcnt(0)
	v_pk_mul_f32 v[24:25], v[16:17], s[32:33] op_sel:[0,1] op_sel_hi:[1,1]
	v_pk_mul_f32 v[26:27], v[18:19], s[32:33] op_sel:[0,1] op_sel_hi:[1,1]
	v_pk_mul_f32 v[28:29], v[20:21], s[40:41] op_sel:[0,1] op_sel_hi:[1,1]
	v_pk_mul_f32 v[30:31], v[22:23], s[40:41] op_sel:[0,1] op_sel_hi:[1,1]
	v_mfma_f32_32x32x16_f16 v[40:55], v[184:187], v[200:203], v[40:55]
	v_cmp_lt_i32_e64 s[60:61], 0, v124
	v_cmp_lt_i32_e64 s[62:63], 0, v125
	v_cmp_lt_i32_e64 s[64:65], 0, v126
	v_cmp_lt_i32_e64 s[66:67], 0, v127
	v_max_f32_e32 v24, v24, v28
	v_max_f32_e32 v25, v25, v29
	v_max_f32_e32 v26, v26, v30
	v_max_f32_e32 v27, v27, v31
	v_cndmask_b32_e64 v24, 0, v24, s[60:61]
	v_cndmask_b32_e64 v25, 0, v25, s[62:63]
	v_cndmask_b32_e64 v26, 0, v26, s[64:65]
	v_cndmask_b32_e64 v27, 0, v27, s[66:67]
	v_mfma_f32_32x32x16_f16 v[56:71], v[184:187], v[204:207], v[56:71]
	v_cvt_pkrtz_f16_f32 v34, v24, v25
	v_cvt_pkrtz_f16_f32 v35, v26, v27
	ds_write2_b64 v5, v[32:33], v[34:35] offset0:0 offset1:66
	s_waitcnt vmcnt(21)
	v_pk_mul_f32 v[24:25], v[16:17], s[34:35] op_sel_hi:[1,0]
	v_pk_mul_f32 v[26:27], v[18:19], s[34:35] op_sel_hi:[1,0]
	v_pk_mul_f32 v[28:29], v[20:21], s[42:43] op_sel_hi:[1,0]
	v_pk_mul_f32 v[30:31], v[22:23], s[42:43] op_sel_hi:[1,0]
	v_mfma_f32_32x32x16_f16 v[72:87], v[184:187], v[12:15], v[72:87]
	v_cmp_lt_i32_e64 s[60:61], 0, v128
	v_cmp_lt_i32_e64 s[62:63], 0, v129
	v_cmp_lt_i32_e64 s[64:65], 0, v130
	v_cmp_lt_i32_e64 s[66:67], 0, v131
	v_max_f32_e32 v24, v24, v28
	v_max_f32_e32 v25, v25, v29
	v_max_f32_e32 v26, v26, v30
	v_max_f32_e32 v27, v27, v31
	v_cndmask_b32_e64 v24, 0, v24, s[60:61]
	v_cndmask_b32_e64 v25, 0, v25, s[62:63]
	v_cndmask_b32_e64 v26, 0, v26, s[64:65]
	v_cndmask_b32_e64 v27, 0, v27, s[66:67]
	v_mfma_f32_32x32x16_f16 v[40:55], v[188:191], v[208:211], v[40:55]
	v_cvt_pkrtz_f16_f32 v32, v24, v25
	v_cvt_pkrtz_f16_f32 v33, v26, v27
	s_waitcnt vmcnt(20)
	v_pk_mul_f32 v[24:25], v[16:17], s[34:35] op_sel:[0,1] op_sel_hi:[1,1]
	v_pk_mul_f32 v[26:27], v[18:19], s[34:35] op_sel:[0,1] op_sel_hi:[1,1]
	v_pk_mul_f32 v[28:29], v[20:21], s[42:43] op_sel:[0,1] op_sel_hi:[1,1]
	v_pk_mul_f32 v[30:31], v[22:23], s[42:43] op_sel:[0,1] op_sel_hi:[1,1]
	v_mfma_f32_32x32x16_f16 v[56:71], v[188:191], v[212:215], v[56:71]
	v_cmp_lt_i32_e64 s[60:61], 0, v132
	v_cmp_lt_i32_e64 s[62:63], 0, v133
	v_cmp_lt_i32_e64 s[64:65], 0, v134
	v_cmp_lt_i32_e64 s[66:67], 0, v135
	v_max_f32_e32 v24, v24, v28
	v_max_f32_e32 v25, v25, v29
	v_max_f32_e32 v26, v26, v30
	v_max_f32_e32 v27, v27, v31
	v_cndmask_b32_e64 v24, 0, v24, s[60:61]
	v_cndmask_b32_e64 v25, 0, v25, s[62:63]
	v_cndmask_b32_e64 v26, 0, v26, s[64:65]
	v_cndmask_b32_e64 v27, 0, v27, s[66:67]
	v_mfma_f32_32x32x16_f16 v[72:87], v[188:191], v[12:15], v[72:87]
	v_cvt_pkrtz_f16_f32 v34, v24, v25
	v_cvt_pkrtz_f16_f32 v35, v26, v27
	ds_write2_b64 v5, v[32:33], v[34:35] offset0:132 offset1:198
	s_waitcnt vmcnt(19)
	v_pk_mul_f32 v[24:25], v[16:17], s[36:37] op_sel_hi:[1,0]
	v_pk_mul_f32 v[26:27], v[18:19], s[36:37] op_sel_hi:[1,0]
	v_pk_mul_f32 v[28:29], v[20:21], s[44:45] op_sel_hi:[1,0]
	v_pk_mul_f32 v[30:31], v[22:23], s[44:45] op_sel_hi:[1,0]
	v_mfma_f32_32x32x16_f16 v[40:55], v[192:195], v[216:219], v[40:55]
	v_cmp_lt_i32_e64 s[60:61], 0, v136
	v_cmp_lt_i32_e64 s[62:63], 0, v137
	v_cmp_lt_i32_e64 s[64:65], 0, v138
	v_cmp_lt_i32_e64 s[66:67], 0, v139
	v_max_f32_e32 v24, v24, v28
	v_max_f32_e32 v25, v25, v29
	v_max_f32_e32 v26, v26, v30
	v_max_f32_e32 v27, v27, v31
	v_cndmask_b32_e64 v24, 0, v24, s[60:61]
	v_cndmask_b32_e64 v25, 0, v25, s[62:63]
	v_cndmask_b32_e64 v26, 0, v26, s[64:65]
	v_cndmask_b32_e64 v27, 0, v27, s[66:67]
	v_mfma_f32_32x32x16_f16 v[56:71], v[192:195], v[220:223], v[56:71]
	v_cvt_pkrtz_f16_f32 v32, v24, v25
	v_cvt_pkrtz_f16_f32 v33, v26, v27
	s_waitcnt vmcnt(18)
	v_pk_mul_f32 v[24:25], v[16:17], s[36:37] op_sel:[0,1] op_sel_hi:[1,1]
	v_pk_mul_f32 v[26:27], v[18:19], s[36:37] op_sel:[0,1] op_sel_hi:[1,1]
	v_pk_mul_f32 v[28:29], v[20:21], s[44:45] op_sel:[0,1] op_sel_hi:[1,1]
	v_pk_mul_f32 v[30:31], v[22:23], s[44:45] op_sel:[0,1] op_sel_hi:[1,1]
	v_mfma_f32_32x32x16_f16 v[72:87], v[192:195], v[12:15], v[72:87]
	v_cmp_lt_i32_e64 s[60:61], 0, v140
	v_cmp_lt_i32_e64 s[62:63], 0, v141
	v_cmp_lt_i32_e64 s[64:65], 0, v142
	v_cmp_lt_i32_e64 s[66:67], 0, v143
	v_max_f32_e32 v24, v24, v28
	v_max_f32_e32 v25, v25, v29
	v_max_f32_e32 v26, v26, v30
	v_max_f32_e32 v27, v27, v31
	v_cndmask_b32_e64 v24, 0, v24, s[60:61]
	v_cndmask_b32_e64 v25, 0, v25, s[62:63]
	v_cndmask_b32_e64 v26, 0, v26, s[64:65]
	v_cndmask_b32_e64 v27, 0, v27, s[66:67]
	v_mfma_f32_32x32x16_f16 v[40:55], v[196:199], v[224:227], v[40:55]
	v_cvt_pkrtz_f16_f32 v34, v24, v25
	v_cvt_pkrtz_f16_f32 v35, v26, v27
	ds_write2_b64 v6, v[32:33], v[34:35] offset0:0 offset1:66
	s_waitcnt vmcnt(17)
	v_pk_mul_f32 v[24:25], v[16:17], s[38:39] op_sel_hi:[1,0]
	v_pk_mul_f32 v[26:27], v[18:19], s[38:39] op_sel_hi:[1,0]
	v_pk_mul_f32 v[28:29], v[20:21], s[46:47] op_sel_hi:[1,0]
	v_pk_mul_f32 v[30:31], v[22:23], s[46:47] op_sel_hi:[1,0]
	v_mfma_f32_32x32x16_f16 v[56:71], v[196:199], v[228:231], v[56:71]
	v_cmp_lt_i32_e64 s[60:61], 0, v144
	v_cmp_lt_i32_e64 s[62:63], 0, v145
	v_cmp_lt_i32_e64 s[64:65], 0, v146
	v_cmp_lt_i32_e64 s[66:67], 0, v147
	v_max_f32_e32 v24, v24, v28
	v_max_f32_e32 v25, v25, v29
	v_max_f32_e32 v26, v26, v30
	v_max_f32_e32 v27, v27, v31
	v_cndmask_b32_e64 v24, 0, v24, s[60:61]
	v_cndmask_b32_e64 v25, 0, v25, s[62:63]
	v_cndmask_b32_e64 v26, 0, v26, s[64:65]
	v_cndmask_b32_e64 v27, 0, v27, s[66:67]
	v_cvt_pkrtz_f16_f32 v32, v24, v25
	v_cvt_pkrtz_f16_f32 v33, v26, v27
	s_waitcnt vmcnt(16)
	v_pk_mul_f32 v[24:25], v[16:17], s[38:39] op_sel:[0,1] op_sel_hi:[1,1]
	v_pk_mul_f32 v[26:27], v[18:19], s[38:39] op_sel:[0,1] op_sel_hi:[1,1]
	v_pk_mul_f32 v[28:29], v[20:21], s[46:47] op_sel:[0,1] op_sel_hi:[1,1]
	v_pk_mul_f32 v[30:31], v[22:23], s[46:47] op_sel:[0,1] op_sel_hi:[1,1]
	v_mfma_f32_32x32x16_f16 v[72:87], v[196:199], v[12:15], v[72:87]
	v_cmp_lt_i32_e64 s[60:61], 0, v148
	v_cmp_lt_i32_e64 s[62:63], 0, v149
	v_cmp_lt_i32_e64 s[64:65], 0, v150
	v_cmp_lt_i32_e64 s[66:67], 0, v151
	v_max_f32_e32 v24, v24, v28
	v_max_f32_e32 v25, v25, v29
	v_max_f32_e32 v26, v26, v30
	v_max_f32_e32 v27, v27, v31
	v_cndmask_b32_e64 v24, 0, v24, s[60:61]
	v_cndmask_b32_e64 v25, 0, v25, s[62:63]
	v_cndmask_b32_e64 v26, 0, v26, s[64:65]
	v_cndmask_b32_e64 v27, 0, v27, s[66:67]
	v_cvt_pkrtz_f16_f32 v34, v24, v25
	v_cvt_pkrtz_f16_f32 v35, v26, v27
	ds_write2_b64 v6, v[32:33], v[34:35] offset0:132 offset1:198
	s_waitcnt vmcnt(12)
	ds_write_b128 v9, v[168:171] offset:32768
	ds_write_b128 v9, v[172:175] offset:33792
	ds_write_b128 v9, v[176:179] offset:34816
	ds_write_b128 v9, v[180:183] offset:35840
	s_add_u32 s3, s19, 6
	s_and_b32 s3, s3, 7
	s_lshl_b32 s3, s3, 10
	v_add_u32_e32 v11, s3, v10
	ds_read_b128 v[16:19], v11
	ds_read_b128 v[20:23], v11 offset:8192
	s_waitcnt lgkmcnt(0)
	s_barrier
	ds_read_b128 v[184:187], v7 offset:33792
	ds_read_b128 v[200:203], v8 offset:32768
	ds_read_b128 v[204:207], v8 offset:33792
	ds_read_b128 v[188:191], v7 offset:33824
	ds_read_b128 v[208:211], v8 offset:34816
	ds_read_b128 v[212:215], v8 offset:35840
	ds_read_b128 v[192:195], v7 offset:33856
	ds_read_b128 v[216:219], v8 offset:36864
	ds_read_b128 v[220:223], v8 offset:37888
	ds_read_b128 v[196:199], v7 offset:33888
	ds_read_b128 v[224:227], v8 offset:38912
	ds_read_b128 v[228:231], v8 offset:39936
	s_add_u32 s3, s19, 7
	s_and_b32 s3, s3, 7
	s_lshl_b32 s57, s3, 10
	s_add_u32 s48, s57, s22
	s_add_u32 s49, s48, 0x2000
	s_add_u32 s50, s48, 0x4000
	s_add_u32 s51, s48, 0x6000
	s_add_u32 s52, s48, 0x8000
	s_add_u32 s53, s48, 0xa000
	s_add_u32 s54, s48, 0xc000
	s_add_u32 s55, s48, 0xe000
	s_lshl_b32 s56, s3, 15
	s_add_u32 s56, s56, s23
	buffer_load_dwordx4 v[120:123], v1, s[4:7], s48 offen nt
	buffer_load_dwordx4 v[124:127], v1, s[4:7], s49 offen nt
	buffer_load_dwordx4 v[128:131], v1, s[4:7], s50 offen nt
	buffer_load_dwordx4 v[132:135], v1, s[4:7], s51 offen nt
	buffer_load_dwordx4 v[136:139], v1, s[4:7], s52 offen nt
	buffer_load_dwordx4 v[140:143], v1, s[4:7], s53 offen nt
	buffer_load_dwordx4 v[144:147], v1, s[4:7], s54 offen nt
	buffer_load_dwordx4 v[148:151], v1, s[4:7], s55 offen nt
	buffer_load_dwordx4 v[168:171], v1, s[8:11], s56 offen
	buffer_load_dwordx4 v[172:175], v1, s[8:11], s56 offen offset:1024
	buffer_load_dwordx4 v[176:179], v1, s[8:11], s56 offen offset:2048
	buffer_load_dwordx4 v[180:183], v1, s[8:11], s56 offen offset:3072
	s_waitcnt vmcnt(23)
	v_pk_mul_f32 v[24:25], v[16:17], s[32:33] op_sel_hi:[1,0]
	v_pk_mul_f32 v[26:27], v[18:19], s[32:33] op_sel_hi:[1,0]
	v_pk_mul_f32 v[28:29], v[20:21], s[40:41] op_sel_hi:[1,0]
	v_pk_mul_f32 v[30:31], v[22:23], s[40:41] op_sel_hi:[1,0]
	v_cmp_lt_i32_e64 s[60:61], 0, v88
	v_cmp_lt_i32_e64 s[62:63], 0, v89
	v_cmp_lt_i32_e64 s[64:65], 0, v90
	v_cmp_lt_i32_e64 s[66:67], 0, v91
	v_max_f32_e32 v24, v24, v28
	v_max_f32_e32 v25, v25, v29
	v_max_f32_e32 v26, v26, v30
	v_max_f32_e32 v27, v27, v31
	v_cndmask_b32_e64 v24, 0, v24, s[60:61]
	v_cndmask_b32_e64 v25, 0, v25, s[62:63]
	v_cndmask_b32_e64 v26, 0, v26, s[64:65]
	v_cndmask_b32_e64 v27, 0, v27, s[66:67]
	v_cvt_pkrtz_f16_f32 v32, v24, v25
	v_cvt_pkrtz_f16_f32 v33, v26, v27
	s_waitcnt vmcnt(22)
	s_waitcnt lgkmcnt(0)
	v_pk_mul_f32 v[24:25], v[16:17], s[32:33] op_sel:[0,1] op_sel_hi:[1,1]
	v_pk_mul_f32 v[26:27], v[18:19], s[32:33] op_sel:[0,1] op_sel_hi:[1,1]
	v_pk_mul_f32 v[28:29], v[20:21], s[40:41] op_sel:[0,1] op_sel_hi:[1,1]
	v_pk_mul_f32 v[30:31], v[22:23], s[40:41] op_sel:[0,1] op_sel_hi:[1,1]
	v_mfma_f32_32x32x16_f16 v[40:55], v[184:187], v[200:203], v[40:55]
	v_cmp_lt_i32_e64 s[60:61], 0, v92
	v_cmp_lt_i32_e64 s[62:63], 0, v93
	v_cmp_lt_i32_e64 s[64:65], 0, v94
	v_cmp_lt_i32_e64 s[66:67], 0, v95
	v_max_f32_e32 v24, v24, v28
	v_max_f32_e32 v25, v25, v29
	v_max_f32_e32 v26, v26, v30
	v_max_f32_e32 v27, v27, v31
	v_cndmask_b32_e64 v24, 0, v24, s[60:61]
	v_cndmask_b32_e64 v25, 0, v25, s[62:63]
	v_cndmask_b32_e64 v26, 0, v26, s[64:65]
	v_cndmask_b32_e64 v27, 0, v27, s[66:67]
	v_mfma_f32_32x32x16_f16 v[56:71], v[184:187], v[204:207], v[56:71]
	v_cvt_pkrtz_f16_f32 v34, v24, v25
	v_cvt_pkrtz_f16_f32 v35, v26, v27
	ds_write2_b64 v3, v[32:33], v[34:35] offset0:0 offset1:66
	s_waitcnt vmcnt(21)
	v_pk_mul_f32 v[24:25], v[16:17], s[34:35] op_sel_hi:[1,0]
	v_pk_mul_f32 v[26:27], v[18:19], s[34:35] op_sel_hi:[1,0]
	v_pk_mul_f32 v[28:29], v[20:21], s[42:43] op_sel_hi:[1,0]
	v_pk_mul_f32 v[30:31], v[22:23], s[42:43] op_sel_hi:[1,0]
	v_mfma_f32_32x32x16_f16 v[72:87], v[184:187], v[12:15], v[72:87]
	v_cmp_lt_i32_e64 s[60:61], 0, v96
	v_cmp_lt_i32_e64 s[62:63], 0, v97
	v_cmp_lt_i32_e64 s[64:65], 0, v98
	v_cmp_lt_i32_e64 s[66:67], 0, v99
	v_max_f32_e32 v24, v24, v28
	v_max_f32_e32 v25, v25, v29
	v_max_f32_e32 v26, v26, v30
	v_max_f32_e32 v27, v27, v31
	v_cndmask_b32_e64 v24, 0, v24, s[60:61]
	v_cndmask_b32_e64 v25, 0, v25, s[62:63]
	v_cndmask_b32_e64 v26, 0, v26, s[64:65]
	v_cndmask_b32_e64 v27, 0, v27, s[66:67]
	v_mfma_f32_32x32x16_f16 v[40:55], v[188:191], v[208:211], v[40:55]
	v_cvt_pkrtz_f16_f32 v32, v24, v25
	v_cvt_pkrtz_f16_f32 v33, v26, v27
	s_waitcnt vmcnt(20)
	v_pk_mul_f32 v[24:25], v[16:17], s[34:35] op_sel:[0,1] op_sel_hi:[1,1]
	v_pk_mul_f32 v[26:27], v[18:19], s[34:35] op_sel:[0,1] op_sel_hi:[1,1]
	v_pk_mul_f32 v[28:29], v[20:21], s[42:43] op_sel:[0,1] op_sel_hi:[1,1]
	v_pk_mul_f32 v[30:31], v[22:23], s[42:43] op_sel:[0,1] op_sel_hi:[1,1]
	v_mfma_f32_32x32x16_f16 v[56:71], v[188:191], v[212:215], v[56:71]
	v_cmp_lt_i32_e64 s[60:61], 0, v100
	v_cmp_lt_i32_e64 s[62:63], 0, v101
	v_cmp_lt_i32_e64 s[64:65], 0, v102
	v_cmp_lt_i32_e64 s[66:67], 0, v103
	v_max_f32_e32 v24, v24, v28
	v_max_f32_e32 v25, v25, v29
	v_max_f32_e32 v26, v26, v30
	v_max_f32_e32 v27, v27, v31
	v_cndmask_b32_e64 v24, 0, v24, s[60:61]
	v_cndmask_b32_e64 v25, 0, v25, s[62:63]
	v_cndmask_b32_e64 v26, 0, v26, s[64:65]
	v_cndmask_b32_e64 v27, 0, v27, s[66:67]
	v_mfma_f32_32x32x16_f16 v[72:87], v[188:191], v[12:15], v[72:87]
	v_cvt_pkrtz_f16_f32 v34, v24, v25
	v_cvt_pkrtz_f16_f32 v35, v26, v27
	ds_write2_b64 v3, v[32:33], v[34:35] offset0:132 offset1:198
	s_waitcnt vmcnt(19)
	v_pk_mul_f32 v[24:25], v[16:17], s[36:37] op_sel_hi:[1,0]
	v_pk_mul_f32 v[26:27], v[18:19], s[36:37] op_sel_hi:[1,0]
	v_pk_mul_f32 v[28:29], v[20:21], s[44:45] op_sel_hi:[1,0]
	v_pk_mul_f32 v[30:31], v[22:23], s[44:45] op_sel_hi:[1,0]
	v_mfma_f32_32x32x16_f16 v[40:55], v[192:195], v[216:219], v[40:55]
	v_cmp_lt_i32_e64 s[60:61], 0, v104
	v_cmp_lt_i32_e64 s[62:63], 0, v105
	v_cmp_lt_i32_e64 s[64:65], 0, v106
	v_cmp_lt_i32_e64 s[66:67], 0, v107
	v_max_f32_e32 v24, v24, v28
	v_max_f32_e32 v25, v25, v29
	v_max_f32_e32 v26, v26, v30
	v_max_f32_e32 v27, v27, v31
	v_cndmask_b32_e64 v24, 0, v24, s[60:61]
	v_cndmask_b32_e64 v25, 0, v25, s[62:63]
	v_cndmask_b32_e64 v26, 0, v26, s[64:65]
	v_cndmask_b32_e64 v27, 0, v27, s[66:67]
	v_mfma_f32_32x32x16_f16 v[56:71], v[192:195], v[220:223], v[56:71]
	v_cvt_pkrtz_f16_f32 v32, v24, v25
	v_cvt_pkrtz_f16_f32 v33, v26, v27
	s_waitcnt vmcnt(18)
	v_pk_mul_f32 v[24:25], v[16:17], s[36:37] op_sel:[0,1] op_sel_hi:[1,1]
	v_pk_mul_f32 v[26:27], v[18:19], s[36:37] op_sel:[0,1] op_sel_hi:[1,1]
	v_pk_mul_f32 v[28:29], v[20:21], s[44:45] op_sel:[0,1] op_sel_hi:[1,1]
	v_pk_mul_f32 v[30:31], v[22:23], s[44:45] op_sel:[0,1] op_sel_hi:[1,1]
	v_mfma_f32_32x32x16_f16 v[72:87], v[192:195], v[12:15], v[72:87]
	v_cmp_lt_i32_e64 s[60:61], 0, v108
	v_cmp_lt_i32_e64 s[62:63], 0, v109
	v_cmp_lt_i32_e64 s[64:65], 0, v110
	v_cmp_lt_i32_e64 s[66:67], 0, v111
	v_max_f32_e32 v24, v24, v28
	v_max_f32_e32 v25, v25, v29
	v_max_f32_e32 v26, v26, v30
	v_max_f32_e32 v27, v27, v31
	v_cndmask_b32_e64 v24, 0, v24, s[60:61]
	v_cndmask_b32_e64 v25, 0, v25, s[62:63]
	v_cndmask_b32_e64 v26, 0, v26, s[64:65]
	v_cndmask_b32_e64 v27, 0, v27, s[66:67]
	v_mfma_f32_32x32x16_f16 v[40:55], v[196:199], v[224:227], v[40:55]
	v_cvt_pkrtz_f16_f32 v34, v24, v25
	v_cvt_pkrtz_f16_f32 v35, v26, v27
	ds_write2_b64 v4, v[32:33], v[34:35] offset0:0 offset1:66
	s_waitcnt vmcnt(17)
	v_pk_mul_f32 v[24:25], v[16:17], s[38:39] op_sel_hi:[1,0]
	v_pk_mul_f32 v[26:27], v[18:19], s[38:39] op_sel_hi:[1,0]
	v_pk_mul_f32 v[28:29], v[20:21], s[46:47] op_sel_hi:[1,0]
	v_pk_mul_f32 v[30:31], v[22:23], s[46:47] op_sel_hi:[1,0]
	v_mfma_f32_32x32x16_f16 v[56:71], v[196:199], v[228:231], v[56:71]
	v_cmp_lt_i32_e64 s[60:61], 0, v112
	v_cmp_lt_i32_e64 s[62:63], 0, v113
	v_cmp_lt_i32_e64 s[64:65], 0, v114
	v_cmp_lt_i32_e64 s[66:67], 0, v115
	v_max_f32_e32 v24, v24, v28
	v_max_f32_e32 v25, v25, v29
	v_max_f32_e32 v26, v26, v30
	v_max_f32_e32 v27, v27, v31
	v_cndmask_b32_e64 v24, 0, v24, s[60:61]
	v_cndmask_b32_e64 v25, 0, v25, s[62:63]
	v_cndmask_b32_e64 v26, 0, v26, s[64:65]
	v_cndmask_b32_e64 v27, 0, v27, s[66:67]
	v_cvt_pkrtz_f16_f32 v32, v24, v25
	v_cvt_pkrtz_f16_f32 v33, v26, v27
	s_waitcnt vmcnt(16)
	v_pk_mul_f32 v[24:25], v[16:17], s[38:39] op_sel:[0,1] op_sel_hi:[1,1]
	v_pk_mul_f32 v[26:27], v[18:19], s[38:39] op_sel:[0,1] op_sel_hi:[1,1]
	v_pk_mul_f32 v[28:29], v[20:21], s[46:47] op_sel:[0,1] op_sel_hi:[1,1]
	v_pk_mul_f32 v[30:31], v[22:23], s[46:47] op_sel:[0,1] op_sel_hi:[1,1]
	v_mfma_f32_32x32x16_f16 v[72:87], v[196:199], v[12:15], v[72:87]
	v_cmp_lt_i32_e64 s[60:61], 0, v116
	v_cmp_lt_i32_e64 s[62:63], 0, v117
	v_cmp_lt_i32_e64 s[64:65], 0, v118
	v_cmp_lt_i32_e64 s[66:67], 0, v119
	v_max_f32_e32 v24, v24, v28
	v_max_f32_e32 v25, v25, v29
	v_max_f32_e32 v26, v26, v30
	v_max_f32_e32 v27, v27, v31
	v_cndmask_b32_e64 v24, 0, v24, s[60:61]
	v_cndmask_b32_e64 v25, 0, v25, s[62:63]
	v_cndmask_b32_e64 v26, 0, v26, s[64:65]
	v_cndmask_b32_e64 v27, 0, v27, s[66:67]
	v_cvt_pkrtz_f16_f32 v34, v24, v25
	v_cvt_pkrtz_f16_f32 v35, v26, v27
	ds_write2_b64 v4, v[32:33], v[34:35] offset0:132 offset1:198
	s_waitcnt vmcnt(12)
	ds_write_b128 v9, v[152:155] offset:0
	ds_write_b128 v9, v[156:159] offset:1024
	ds_write_b128 v9, v[160:163] offset:2048
	ds_write_b128 v9, v[164:167] offset:3072
	s_add_u32 s3, s19, 7
	s_and_b32 s3, s3, 7
	s_lshl_b32 s3, s3, 10
	v_add_u32_e32 v11, s3, v10
	ds_read_b128 v[16:19], v11
	ds_read_b128 v[20:23], v11 offset:8192
	s_waitcnt lgkmcnt(0)
	s_barrier
	ds_read_b128 v[184:187], v7 offset:0
	ds_read_b128 v[200:203], v8 offset:0
	ds_read_b128 v[204:207], v8 offset:1024
	ds_read_b128 v[188:191], v7 offset:32
	ds_read_b128 v[208:211], v8 offset:2048
	ds_read_b128 v[212:215], v8 offset:3072
	ds_read_b128 v[192:195], v7 offset:64
	ds_read_b128 v[216:219], v8 offset:4096
	ds_read_b128 v[220:223], v8 offset:5120
	ds_read_b128 v[196:199], v7 offset:96
	ds_read_b128 v[224:227], v8 offset:6144
	ds_read_b128 v[228:231], v8 offset:7168
	s_waitcnt vmcnt(11)
	v_pk_mul_f32 v[24:25], v[16:17], s[32:33] op_sel_hi:[1,0]
	v_pk_mul_f32 v[26:27], v[18:19], s[32:33] op_sel_hi:[1,0]
	v_pk_mul_f32 v[28:29], v[20:21], s[40:41] op_sel_hi:[1,0]
	v_pk_mul_f32 v[30:31], v[22:23], s[40:41] op_sel_hi:[1,0]
	v_cmp_lt_i32_e64 s[60:61], 0, v120
	v_cmp_lt_i32_e64 s[62:63], 0, v121
	v_cmp_lt_i32_e64 s[64:65], 0, v122
	v_cmp_lt_i32_e64 s[66:67], 0, v123
	v_max_f32_e32 v24, v24, v28
	v_max_f32_e32 v25, v25, v29
	v_max_f32_e32 v26, v26, v30
	v_max_f32_e32 v27, v27, v31
	v_cndmask_b32_e64 v24, 0, v24, s[60:61]
	v_cndmask_b32_e64 v25, 0, v25, s[62:63]
	v_cndmask_b32_e64 v26, 0, v26, s[64:65]
	v_cndmask_b32_e64 v27, 0, v27, s[66:67]
	v_cvt_pkrtz_f16_f32 v32, v24, v25
	v_cvt_pkrtz_f16_f32 v33, v26, v27
	s_waitcnt vmcnt(10)
	s_waitcnt lgkmcnt(0)
	v_pk_mul_f32 v[24:25], v[16:17], s[32:33] op_sel:[0,1] op_sel_hi:[1,1]
	v_pk_mul_f32 v[26:27], v[18:19], s[32:33] op_sel:[0,1] op_sel_hi:[1,1]
	v_pk_mul_f32 v[28:29], v[20:21], s[40:41] op_sel:[0,1] op_sel_hi:[1,1]
	v_pk_mul_f32 v[30:31], v[22:23], s[40:41] op_sel:[0,1] op_sel_hi:[1,1]
	v_mfma_f32_32x32x16_f16 v[40:55], v[184:187], v[200:203], v[40:55]
	v_cmp_lt_i32_e64 s[60:61], 0, v124
	v_cmp_lt_i32_e64 s[62:63], 0, v125
	v_cmp_lt_i32_e64 s[64:65], 0, v126
	v_cmp_lt_i32_e64 s[66:67], 0, v127
	v_max_f32_e32 v24, v24, v28
	v_max_f32_e32 v25, v25, v29
	v_max_f32_e32 v26, v26, v30
	v_max_f32_e32 v27, v27, v31
	v_cndmask_b32_e64 v24, 0, v24, s[60:61]
	v_cndmask_b32_e64 v25, 0, v25, s[62:63]
	v_cndmask_b32_e64 v26, 0, v26, s[64:65]
	v_cndmask_b32_e64 v27, 0, v27, s[66:67]
	v_mfma_f32_32x32x16_f16 v[56:71], v[184:187], v[204:207], v[56:71]
	v_cvt_pkrtz_f16_f32 v34, v24, v25
	v_cvt_pkrtz_f16_f32 v35, v26, v27
	ds_write2_b64 v5, v[32:33], v[34:35] offset0:0 offset1:66
	s_waitcnt vmcnt(9)
	v_pk_mul_f32 v[24:25], v[16:17], s[34:35] op_sel_hi:[1,0]
	v_pk_mul_f32 v[26:27], v[18:19], s[34:35] op_sel_hi:[1,0]
	v_pk_mul_f32 v[28:29], v[20:21], s[42:43] op_sel_hi:[1,0]
	v_pk_mul_f32 v[30:31], v[22:23], s[42:43] op_sel_hi:[1,0]
	v_mfma_f32_32x32x16_f16 v[72:87], v[184:187], v[12:15], v[72:87]
	v_cmp_lt_i32_e64 s[60:61], 0, v128
	v_cmp_lt_i32_e64 s[62:63], 0, v129
	v_cmp_lt_i32_e64 s[64:65], 0, v130
	v_cmp_lt_i32_e64 s[66:67], 0, v131
	v_max_f32_e32 v24, v24, v28
	v_max_f32_e32 v25, v25, v29
	v_max_f32_e32 v26, v26, v30
	v_max_f32_e32 v27, v27, v31
	v_cndmask_b32_e64 v24, 0, v24, s[60:61]
	v_cndmask_b32_e64 v25, 0, v25, s[62:63]
	v_cndmask_b32_e64 v26, 0, v26, s[64:65]
	v_cndmask_b32_e64 v27, 0, v27, s[66:67]
	v_mfma_f32_32x32x16_f16 v[40:55], v[188:191], v[208:211], v[40:55]
	v_cvt_pkrtz_f16_f32 v32, v24, v25
	v_cvt_pkrtz_f16_f32 v33, v26, v27
	s_waitcnt vmcnt(8)
	v_pk_mul_f32 v[24:25], v[16:17], s[34:35] op_sel:[0,1] op_sel_hi:[1,1]
	v_pk_mul_f32 v[26:27], v[18:19], s[34:35] op_sel:[0,1] op_sel_hi:[1,1]
	v_pk_mul_f32 v[28:29], v[20:21], s[42:43] op_sel:[0,1] op_sel_hi:[1,1]
	v_pk_mul_f32 v[30:31], v[22:23], s[42:43] op_sel:[0,1] op_sel_hi:[1,1]
	v_mfma_f32_32x32x16_f16 v[56:71], v[188:191], v[212:215], v[56:71]
	v_cmp_lt_i32_e64 s[60:61], 0, v132
	v_cmp_lt_i32_e64 s[62:63], 0, v133
	v_cmp_lt_i32_e64 s[64:65], 0, v134
	v_cmp_lt_i32_e64 s[66:67], 0, v135
	v_max_f32_e32 v24, v24, v28
	v_max_f32_e32 v25, v25, v29
	v_max_f32_e32 v26, v26, v30
	v_max_f32_e32 v27, v27, v31
	v_cndmask_b32_e64 v24, 0, v24, s[60:61]
	v_cndmask_b32_e64 v25, 0, v25, s[62:63]
	v_cndmask_b32_e64 v26, 0, v26, s[64:65]
	v_cndmask_b32_e64 v27, 0, v27, s[66:67]
	v_mfma_f32_32x32x16_f16 v[72:87], v[188:191], v[12:15], v[72:87]
	v_cvt_pkrtz_f16_f32 v34, v24, v25
	v_cvt_pkrtz_f16_f32 v35, v26, v27
	ds_write2_b64 v5, v[32:33], v[34:35] offset0:132 offset1:198
	s_waitcnt vmcnt(7)
	v_pk_mul_f32 v[24:25], v[16:17], s[36:37] op_sel_hi:[1,0]
	v_pk_mul_f32 v[26:27], v[18:19], s[36:37] op_sel_hi:[1,0]
	v_pk_mul_f32 v[28:29], v[20:21], s[44:45] op_sel_hi:[1,0]
	v_pk_mul_f32 v[30:31], v[22:23], s[44:45] op_sel_hi:[1,0]
	v_mfma_f32_32x32x16_f16 v[40:55], v[192:195], v[216:219], v[40:55]
	v_cmp_lt_i32_e64 s[60:61], 0, v136
	v_cmp_lt_i32_e64 s[62:63], 0, v137
	v_cmp_lt_i32_e64 s[64:65], 0, v138
	v_cmp_lt_i32_e64 s[66:67], 0, v139
	v_max_f32_e32 v24, v24, v28
	v_max_f32_e32 v25, v25, v29
	v_max_f32_e32 v26, v26, v30
	v_max_f32_e32 v27, v27, v31
	v_cndmask_b32_e64 v24, 0, v24, s[60:61]
	v_cndmask_b32_e64 v25, 0, v25, s[62:63]
	v_cndmask_b32_e64 v26, 0, v26, s[64:65]
	v_cndmask_b32_e64 v27, 0, v27, s[66:67]
	v_mfma_f32_32x32x16_f16 v[56:71], v[192:195], v[220:223], v[56:71]
	v_cvt_pkrtz_f16_f32 v32, v24, v25
	v_cvt_pkrtz_f16_f32 v33, v26, v27
	s_waitcnt vmcnt(6)
	v_pk_mul_f32 v[24:25], v[16:17], s[36:37] op_sel:[0,1] op_sel_hi:[1,1]
	v_pk_mul_f32 v[26:27], v[18:19], s[36:37] op_sel:[0,1] op_sel_hi:[1,1]
	v_pk_mul_f32 v[28:29], v[20:21], s[44:45] op_sel:[0,1] op_sel_hi:[1,1]
	v_pk_mul_f32 v[30:31], v[22:23], s[44:45] op_sel:[0,1] op_sel_hi:[1,1]
	v_mfma_f32_32x32x16_f16 v[72:87], v[192:195], v[12:15], v[72:87]
	v_cmp_lt_i32_e64 s[60:61], 0, v140
	v_cmp_lt_i32_e64 s[62:63], 0, v141
	v_cmp_lt_i32_e64 s[64:65], 0, v142
	v_cmp_lt_i32_e64 s[66:67], 0, v143
	v_max_f32_e32 v24, v24, v28
	v_max_f32_e32 v25, v25, v29
	v_max_f32_e32 v26, v26, v30
	v_max_f32_e32 v27, v27, v31
	v_cndmask_b32_e64 v24, 0, v24, s[60:61]
	v_cndmask_b32_e64 v25, 0, v25, s[62:63]
	v_cndmask_b32_e64 v26, 0, v26, s[64:65]
	v_cndmask_b32_e64 v27, 0, v27, s[66:67]
	v_mfma_f32_32x32x16_f16 v[40:55], v[196:199], v[224:227], v[40:55]
	v_cvt_pkrtz_f16_f32 v34, v24, v25
	v_cvt_pkrtz_f16_f32 v35, v26, v27
	ds_write2_b64 v6, v[32:33], v[34:35] offset0:0 offset1:66
	s_waitcnt vmcnt(5)
	v_pk_mul_f32 v[24:25], v[16:17], s[38:39] op_sel_hi:[1,0]
	v_pk_mul_f32 v[26:27], v[18:19], s[38:39] op_sel_hi:[1,0]
	v_pk_mul_f32 v[28:29], v[20:21], s[46:47] op_sel_hi:[1,0]
	v_pk_mul_f32 v[30:31], v[22:23], s[46:47] op_sel_hi:[1,0]
	v_mfma_f32_32x32x16_f16 v[56:71], v[196:199], v[228:231], v[56:71]
	v_cmp_lt_i32_e64 s[60:61], 0, v144
	v_cmp_lt_i32_e64 s[62:63], 0, v145
	v_cmp_lt_i32_e64 s[64:65], 0, v146
	v_cmp_lt_i32_e64 s[66:67], 0, v147
	v_max_f32_e32 v24, v24, v28
	v_max_f32_e32 v25, v25, v29
	v_max_f32_e32 v26, v26, v30
	v_max_f32_e32 v27, v27, v31
	v_cndmask_b32_e64 v24, 0, v24, s[60:61]
	v_cndmask_b32_e64 v25, 0, v25, s[62:63]
	v_cndmask_b32_e64 v26, 0, v26, s[64:65]
	v_cndmask_b32_e64 v27, 0, v27, s[66:67]
	v_cvt_pkrtz_f16_f32 v32, v24, v25
	v_cvt_pkrtz_f16_f32 v33, v26, v27
	s_waitcnt vmcnt(4)
	v_pk_mul_f32 v[24:25], v[16:17], s[38:39] op_sel:[0,1] op_sel_hi:[1,1]
	v_pk_mul_f32 v[26:27], v[18:19], s[38:39] op_sel:[0,1] op_sel_hi:[1,1]
	v_pk_mul_f32 v[28:29], v[20:21], s[46:47] op_sel:[0,1] op_sel_hi:[1,1]
	v_pk_mul_f32 v[30:31], v[22:23], s[46:47] op_sel:[0,1] op_sel_hi:[1,1]
	v_mfma_f32_32x32x16_f16 v[72:87], v[196:199], v[12:15], v[72:87]
	v_cmp_lt_i32_e64 s[60:61], 0, v148
	v_cmp_lt_i32_e64 s[62:63], 0, v149
	v_cmp_lt_i32_e64 s[64:65], 0, v150
	v_cmp_lt_i32_e64 s[66:67], 0, v151
	v_max_f32_e32 v24, v24, v28
	v_max_f32_e32 v25, v25, v29
	v_max_f32_e32 v26, v26, v30
	v_max_f32_e32 v27, v27, v31
	v_cndmask_b32_e64 v24, 0, v24, s[60:61]
	v_cndmask_b32_e64 v25, 0, v25, s[62:63]
	v_cndmask_b32_e64 v26, 0, v26, s[64:65]
	v_cndmask_b32_e64 v27, 0, v27, s[66:67]
	v_cvt_pkrtz_f16_f32 v34, v24, v25
	v_cvt_pkrtz_f16_f32 v35, v26, v27
	ds_write2_b64 v6, v[32:33], v[34:35] offset0:132 offset1:198
	s_waitcnt vmcnt(0)
	ds_write_b128 v9, v[168:171] offset:32768
	ds_write_b128 v9, v[172:175] offset:33792
	ds_write_b128 v9, v[176:179] offset:34816
	ds_write_b128 v9, v[180:183] offset:35840
	s_waitcnt lgkmcnt(0)
	s_barrier
	ds_read_b128 v[184:187], v7 offset:33792
	ds_read_b128 v[200:203], v8 offset:32768
	ds_read_b128 v[204:207], v8 offset:33792
	ds_read_b128 v[188:191], v7 offset:33824
	ds_read_b128 v[208:211], v8 offset:34816
	ds_read_b128 v[212:215], v8 offset:35840
	ds_read_b128 v[192:195], v7 offset:33856
	ds_read_b128 v[216:219], v8 offset:36864
	ds_read_b128 v[220:223], v8 offset:37888
	ds_read_b128 v[196:199], v7 offset:33888
	ds_read_b128 v[224:227], v8 offset:38912
	ds_read_b128 v[228:231], v8 offset:39936
	s_waitcnt lgkmcnt(0)
	v_mfma_f32_32x32x16_f16 v[40:55], v[184:187], v[200:203], v[40:55]
	v_mfma_f32_32x32x16_f16 v[56:71], v[184:187], v[204:207], v[56:71]
	v_mfma_f32_32x32x16_f16 v[72:87], v[184:187], v[12:15], v[72:87]
	v_mfma_f32_32x32x16_f16 v[40:55], v[188:191], v[208:211], v[40:55]
	v_mfma_f32_32x32x16_f16 v[56:71], v[188:191], v[212:215], v[56:71]
	v_mfma_f32_32x32x16_f16 v[72:87], v[188:191], v[12:15], v[72:87]
	v_mfma_f32_32x32x16_f16 v[40:55], v[192:195], v[216:219], v[40:55]
	v_mfma_f32_32x32x16_f16 v[56:71], v[192:195], v[220:223], v[56:71]
	v_mfma_f32_32x32x16_f16 v[72:87], v[192:195], v[12:15], v[72:87]
	v_mfma_f32_32x32x16_f16 v[40:55], v[196:199], v[224:227], v[40:55]
	v_mfma_f32_32x32x16_f16 v[56:71], v[196:199], v[228:231], v[56:71]
	v_mfma_f32_32x32x16_f16 v[72:87], v[196:199], v[12:15], v[72:87]
	s_nop 15
	s_barrier
	s_mul_i32 s3, s20, 0xc000
	s_mul_i32 s57, s21, 0xc00
	s_add_u32 s3, s3, s57
	v_add_u32_e32 v36, s3, v1
	ds_write_b128 v36, v[40:43] offset:0
	ds_write_b128 v36, v[56:59] offset:1024
	ds_write_b128 v36, v[72:75] offset:2048
	ds_write_b128 v36, v[44:47] offset:12288
	ds_write_b128 v36, v[60:63] offset:13312
	ds_write_b128 v36, v[76:79] offset:14336
	ds_write_b128 v36, v[48:51] offset:24576
	ds_write_b128 v36, v[64:67] offset:25600
	ds_write_b128 v36, v[80:83] offset:26624
	ds_write_b128 v36, v[52:55] offset:36864
	ds_write_b128 v36, v[68:71] offset:37888
	ds_write_b128 v36, v[84:87] offset:38912
	s_waitcnt lgkmcnt(0)
	s_barrier
	s_mul_i32 s3, s16, 0x3000
	v_add_u32_e32 v36, s3, v1
	ds_read_b128 v[40:43], v36 offset:0
	ds_read_b128 v[44:47], v36 offset:1024
	ds_read_b128 v[48:51], v36 offset:2048
	ds_read_b128 v[52:55], v36 offset:3072
	ds_read_b128 v[56:59], v36 offset:4096
	ds_read_b128 v[60:63], v36 offset:5120
	ds_read_b128 v[64:67], v36 offset:6144
	ds_read_b128 v[68:71], v36 offset:7168
	ds_read_b128 v[72:75], v36 offset:8192
	ds_read_b128 v[76:79], v36 offset:9216
	ds_read_b128 v[80:83], v36 offset:10240
	ds_read_b128 v[84:87], v36 offset:11264
	s_waitcnt lgkmcnt(0)
	v_add_f32_e32 v40, v40, v52
	v_add_f32_e32 v41, v41, v53
	v_add_f32_e32 v42, v42, v54
	v_add_f32_e32 v43, v43, v55
	v_add_f32_e32 v44, v44, v56
	v_add_f32_e32 v45, v45, v57
	v_add_f32_e32 v46, v46, v58
	v_add_f32_e32 v47, v47, v59
	v_add_f32_e32 v48, v48, v60
	v_add_f32_e32 v49, v49, v61
	v_add_f32_e32 v50, v50, v62
	v_add_f32_e32 v51, v51, v63
	v_add_f32_e32 v40, v40, v64
	v_add_f32_e32 v41, v41, v65
	v_add_f32_e32 v42, v42, v66
	v_add_f32_e32 v43, v43, v67
	v_add_f32_e32 v44, v44, v68
	v_add_f32_e32 v45, v45, v69
	v_add_f32_e32 v46, v46, v70
	v_add_f32_e32 v47, v47, v71
	v_add_f32_e32 v48, v48, v72
	v_add_f32_e32 v49, v49, v73
	v_add_f32_e32 v50, v50, v74
	v_add_f32_e32 v51, v51, v75
	v_add_f32_e32 v40, v40, v76
	v_add_f32_e32 v41, v41, v77
	v_add_f32_e32 v42, v42, v78
	v_add_f32_e32 v43, v43, v79
	v_add_f32_e32 v44, v44, v80
	v_add_f32_e32 v45, v45, v81
	v_add_f32_e32 v46, v46, v82
	v_add_f32_e32 v47, v47, v83
	v_add_f32_e32 v48, v48, v84
	v_add_f32_e32 v49, v49, v85
	v_add_f32_e32 v50, v50, v86
	v_add_f32_e32 v51, v51, v87
	v_cmp_eq_f32_e64 s[60:61], 0, v48
	v_cmp_eq_f32_e64 s[62:63], 0, v49
	v_cmp_eq_f32_e64 s[64:65], 0, v50
	v_cmp_eq_f32_e64 s[66:67], 0, v51
	s_nop 3
	s_or_b64 s[60:61], s[60:61], s[62:63]
	s_or_b64 s[64:65], s[64:65], s[66:67]
	s_or_b64 s[60:61], s[60:61], s[64:65]
	s_cmp_eq_u64 s[60:61], 0
	s_cbranch_scc1 .Lgm_no_fallback
	v_and_b32_e32 v101, 31, v2
	v_lshlrev_b32_e32 v101, 4, v101
	v_mov_b32_e32 v88, 0
	v_mov_b32_e32 v89, 0
	s_mov_b32 s3, 0
